# GEMM K-loops: loop-top LDS fragment reads issued in phase 8 of the previous iteration (all 4 loops); P1 per-iteration vmcnt(0) drain removed
# speedup vs baseline: 1.0053x; 1.0053x over previous
.LBB0_191:
	s_ashr_i32 s61, s60, 31
	s_lshl_b64 s[62:63], s[60:61], 19
	s_add_u32 s62, s12, s62
	s_addc_u32 s63, s13, s63
	s_ashr_i32 s59, s58, 31
	s_lshl_b64 s[64:65], s[58:59], 19
	s_add_u32 s64, s14, s64
	s_addc_u32 s65, s15, s65
	s_andn2_b64 vcc, exec, s[30:31]
	s_cbranch_vccnz .LBB0_195
	v_cmp_lt_i64_e32 vcc, s[68:69], v[142:143]
	s_and_b64 s[68:69], vcc, exec
	s_cselect_b32 s9, s63, s11
	s_cselect_b32 s59, s62, s10
	s_cselect_b32 s61, s65, s67
	s_cselect_b32 s86, s64, s66
	s_add_u32 s10, s10, 0x40080
	s_addc_u32 s11, s11, 0
	s_add_u32 s87, s66, 0x100
	s_addc_u32 s88, s67, 0
	s_mov_b32 s66, 0
	s_waitcnt vmcnt(0)
	v_add_u32_e32 v154, s77, v157
	ds_read_b128 v[146:149], v154
	ds_read_b128 v[150:153], v154 offset:1024
	ds_read_b128 v[164:167], v154 offset:2048
	ds_read_b128 v[168:171], v154 offset:3072
	s_add_i32 s89, s66, 2
	s_add_u32 s67, s10, 0xfffc0080
	s_addc_u32 s68, s11, -1
	s_cmp_eq_u32 s75, s66
	s_cselect_b32 s66, s86, s87
	s_cselect_b32 s69, s9, s68
	s_cselect_b32 s68, s59, s67
	s_cselect_b32 s67, s61, s88
	v_lshl_add_u64 v[206:207], s[10:11], 0, v[138:139]
	s_add_i32 m0, s52, 0xc000
	ds_read_b128 v[172:175], v159
	ds_read_b128 v[176:179], v159 offset:1024
	ds_read_b128 v[180:183], v159 offset:2048
	ds_read_b128 v[184:187], v159 offset:3072
	ds_read_b128 v[188:191], v159 offset:4096
	ds_read_b128 v[192:195], v159 offset:5120
	ds_read_b128 v[198:201], v159 offset:6144
	ds_read_b128 v[202:205], v159 offset:7168
	global_load_lds_dwordx4 v[206:207], off
	v_lshl_add_u64 v[206:207], s[10:11], 0, v[140:141]
	s_add_i32 m0, s52, 0xe000
	s_nop 0
	global_load_lds_dwordx4 v[206:207], off
	s_waitcnt lgkmcnt(8)
	s_barrier
	s_setprio 1
	s_waitcnt lgkmcnt(0)
	v_mfma_i32_16x16x64_i8 v[62:65], v[146:149], v[172:175], 0
	v_mfma_i32_16x16x64_i8 v[58:61], v[164:167], v[172:175], 0
	v_mfma_i32_16x16x64_i8 v[54:57], v[146:149], v[180:183], 0
	v_mfma_i32_16x16x64_i8 v[50:53], v[164:167], v[180:183], 0
	v_mfma_i32_16x16x64_i8 v[46:49], v[146:149], v[188:191], 0
	v_mfma_i32_16x16x64_i8 v[42:45], v[164:167], v[188:191], 0
	v_mfma_i32_16x16x64_i8 v[38:41], v[146:149], v[198:201], 0
	v_mfma_i32_16x16x64_i8 v[34:37], v[164:167], v[198:201], 0
	v_mfma_i32_16x16x64_i8 v[62:65], v[150:153], v[176:179], v[62:65]
	v_mfma_i32_16x16x64_i8 v[58:61], v[168:171], v[176:179], v[58:61]
	v_mfma_i32_16x16x64_i8 v[54:57], v[150:153], v[184:187], v[54:57]
	v_mfma_i32_16x16x64_i8 v[50:53], v[168:171], v[184:187], v[50:53]
	v_mfma_i32_16x16x64_i8 v[46:49], v[150:153], v[192:195], v[46:49]
	v_mfma_i32_16x16x64_i8 v[42:45], v[168:171], v[192:195], v[42:45]
	v_mfma_i32_16x16x64_i8 v[38:41], v[150:153], v[202:205], v[38:41]
	v_mfma_i32_16x16x64_i8 v[34:37], v[168:171], v[202:205], v[34:37]
	s_setprio 0
	s_barrier
	s_add_i32 s90, s77, s4
	v_add_u32_e32 v154, s78, v157
	v_lshl_add_u64 v[222:223], s[66:67], 0, v[134:135]
	s_mov_b32 m0, s90
	ds_read_b128 v[206:209], v154
	ds_read_b128 v[210:213], v154 offset:1024
	ds_read_b128 v[214:217], v154 offset:2048
	ds_read_b128 v[218:221], v154 offset:3072
	global_load_lds_dwordx4 v[222:223], off
	v_lshl_add_u64 v[224:225], s[66:67], 0, v[130:131]
	s_add_i32 m0, s90, 0x2000
	s_nop 0
	global_load_lds_dwordx4 v[224:225], off
	s_barrier
	s_setprio 1
	s_waitcnt lgkmcnt(0)
	v_mfma_i32_16x16x64_i8 v[126:129], v[206:209], v[172:175], 0
	v_mfma_i32_16x16x64_i8 v[122:125], v[214:217], v[172:175], 0
	ds_read_b128 v[172:175], v159 offset:16384
	v_mfma_i32_16x16x64_i8 v[118:121], v[206:209], v[180:183], 0
	v_mfma_i32_16x16x64_i8 v[114:117], v[214:217], v[180:183], 0
	ds_read_b128 v[180:183], v159 offset:18432
	v_mfma_i32_16x16x64_i8 v[110:113], v[206:209], v[188:191], 0
	v_mfma_i32_16x16x64_i8 v[106:109], v[214:217], v[188:191], 0
	ds_read_b128 v[188:191], v159 offset:20480
	v_mfma_i32_16x16x64_i8 v[102:105], v[206:209], v[198:201], 0
	v_mfma_i32_16x16x64_i8 v[98:101], v[214:217], v[198:201], 0
	ds_read_b128 v[198:201], v159 offset:22528
	v_mfma_i32_16x16x64_i8 v[126:129], v[210:213], v[176:179], v[126:129]
	v_mfma_i32_16x16x64_i8 v[122:125], v[218:221], v[176:179], v[122:125]
	ds_read_b128 v[176:179], v159 offset:17408
	v_mfma_i32_16x16x64_i8 v[118:121], v[210:213], v[184:187], v[118:121]
	v_mfma_i32_16x16x64_i8 v[114:117], v[218:221], v[184:187], v[114:117]
	ds_read_b128 v[184:187], v159 offset:19456
	v_mfma_i32_16x16x64_i8 v[110:113], v[210:213], v[192:195], v[110:113]
	v_mfma_i32_16x16x64_i8 v[106:109], v[218:221], v[192:195], v[106:109]
	ds_read_b128 v[192:195], v159 offset:21504
	v_mfma_i32_16x16x64_i8 v[102:105], v[210:213], v[202:205], v[102:105]
	v_mfma_i32_16x16x64_i8 v[98:101], v[218:221], v[202:205], v[98:101]
	ds_read_b128 v[202:205], v159 offset:23552
	s_setprio 0
	s_mov_b32 m0, s52
	v_lshl_add_u64 v[226:227], s[68:69], 0, v[136:137]
	s_barrier
	global_load_lds_dwordx4 v[226:227], off
	v_lshl_add_u64 v[228:229], s[68:69], 0, v[132:133]
	s_mov_b32 m0, s53
	s_nop 0
	global_load_lds_dwordx4 v[228:229], off
	s_barrier
	s_setprio 1
	s_waitcnt lgkmcnt(0)
	v_mfma_i32_16x16x64_i8 v[30:33], v[146:149], v[172:175], 0
	v_mfma_i32_16x16x64_i8 v[26:29], v[164:167], v[172:175], 0
	v_mfma_i32_16x16x64_i8 v[22:25], v[146:149], v[180:183], 0
	v_mfma_i32_16x16x64_i8 v[18:21], v[164:167], v[180:183], 0
	v_mfma_i32_16x16x64_i8 v[14:17], v[146:149], v[188:191], 0
	v_mfma_i32_16x16x64_i8 v[10:13], v[164:167], v[188:191], 0
	v_mfma_i32_16x16x64_i8 v[6:9], v[146:149], v[198:201], 0
	v_mfma_i32_16x16x64_i8 v[2:5], v[164:167], v[198:201], 0
	v_mfma_i32_16x16x64_i8 v[30:33], v[150:153], v[176:179], v[30:33]
	v_mfma_i32_16x16x64_i8 v[26:29], v[168:171], v[176:179], v[26:29]
	v_mfma_i32_16x16x64_i8 v[22:25], v[150:153], v[184:187], v[22:25]
	v_mfma_i32_16x16x64_i8 v[18:21], v[168:171], v[184:187], v[18:21]
	v_mfma_i32_16x16x64_i8 v[14:17], v[150:153], v[192:195], v[14:17]
	v_mfma_i32_16x16x64_i8 v[10:13], v[168:171], v[192:195], v[10:13]
	v_mfma_i32_16x16x64_i8 v[6:9], v[150:153], v[202:205], v[6:9]
	v_mfma_i32_16x16x64_i8 v[2:5], v[168:171], v[202:205], v[2:5]
	s_setprio 0
	s_barrier
	s_add_u32 s90, s66, 0x40000
	s_addc_u32 s91, s67, 0
	s_add_i32 s92, s78, s4
	v_lshl_add_u64 v[146:147], s[90:91], 0, v[134:135]
	s_mov_b32 m0, s92
	s_nop 0
	global_load_lds_dwordx4 v[146:147], off
	v_lshl_add_u64 v[146:147], s[90:91], 0, v[130:131]
	s_add_i32 m0, s92, 0x2000
	s_nop 0
	global_load_lds_dwordx4 v[146:147], off
	s_waitcnt vmcnt(6)
	s_barrier
	s_setprio 1
	v_mfma_i32_16x16x64_i8 v[94:97], v[206:209], v[172:175], 0
	v_mfma_i32_16x16x64_i8 v[90:93], v[214:217], v[172:175], 0
	ds_read_b128 v[172:175], v159 offset:32768
	v_mfma_i32_16x16x64_i8 v[86:89], v[206:209], v[180:183], 0
	v_mfma_i32_16x16x64_i8 v[82:85], v[214:217], v[180:183], 0
	ds_read_b128 v[180:183], v159 offset:34816
	v_mfma_i32_16x16x64_i8 v[78:81], v[206:209], v[188:191], 0
	v_mfma_i32_16x16x64_i8 v[74:77], v[214:217], v[188:191], 0
	ds_read_b128 v[188:191], v159 offset:36864
	v_mfma_i32_16x16x64_i8 v[70:73], v[206:209], v[198:201], 0
	v_mfma_i32_16x16x64_i8 v[66:69], v[214:217], v[198:201], 0
	ds_read_b128 v[198:201], v159 offset:38912
	v_mfma_i32_16x16x64_i8 v[94:97], v[210:213], v[176:179], v[94:97]
	v_mfma_i32_16x16x64_i8 v[90:93], v[218:221], v[176:179], v[90:93]
	ds_read_b128 v[176:179], v159 offset:33792
	v_mfma_i32_16x16x64_i8 v[86:89], v[210:213], v[184:187], v[86:89]
	v_mfma_i32_16x16x64_i8 v[82:85], v[218:221], v[184:187], v[82:85]
	ds_read_b128 v[184:187], v159 offset:35840
	v_mfma_i32_16x16x64_i8 v[78:81], v[210:213], v[192:195], v[78:81]
	v_mfma_i32_16x16x64_i8 v[74:77], v[218:221], v[192:195], v[74:77]
	ds_read_b128 v[192:195], v159 offset:37888
	v_mfma_i32_16x16x64_i8 v[70:73], v[210:213], v[202:205], v[70:73]
	v_mfma_i32_16x16x64_i8 v[66:69], v[218:221], v[202:205], v[66:69]
	ds_read_b128 v[202:205], v159 offset:39936
	s_setprio 0
	s_add_i32 s90, 0, 0x18000
	v_add_u32_e32 v154, s90, v157
	s_barrier
	ds_read_b128 v[146:149], v154
	ds_read_b128 v[150:153], v154 offset:1024
	ds_read_b128 v[164:167], v154 offset:2048
	ds_read_b128 v[168:171], v154 offset:3072
	s_add_u32 s68, s68, 0x40000
	s_addc_u32 s69, s69, 0
	s_mov_b32 m0, s54
	v_lshl_add_u64 v[206:207], s[68:69], 0, v[136:137]
	global_load_lds_dwordx4 v[206:207], off
	v_lshl_add_u64 v[206:207], s[68:69], 0, v[132:133]
	s_mov_b32 m0, s55
	s_nop 0
	global_load_lds_dwordx4 v[206:207], off
	s_waitcnt lgkmcnt(8)
	s_barrier
	s_setprio 1
	s_waitcnt lgkmcnt(0)
	v_mfma_i32_16x16x64_i8 v[62:65], v[146:149], v[172:175], v[62:65]
	v_mfma_i32_16x16x64_i8 v[58:61], v[164:167], v[172:175], v[58:61]
	v_mfma_i32_16x16x64_i8 v[54:57], v[146:149], v[180:183], v[54:57]
	v_mfma_i32_16x16x64_i8 v[50:53], v[164:167], v[180:183], v[50:53]
	v_mfma_i32_16x16x64_i8 v[46:49], v[146:149], v[188:191], v[46:49]
	v_mfma_i32_16x16x64_i8 v[42:45], v[164:167], v[188:191], v[42:45]
	v_mfma_i32_16x16x64_i8 v[38:41], v[146:149], v[198:201], v[38:41]
	v_mfma_i32_16x16x64_i8 v[34:37], v[164:167], v[198:201], v[34:37]
	v_mfma_i32_16x16x64_i8 v[62:65], v[150:153], v[176:179], v[62:65]
	v_mfma_i32_16x16x64_i8 v[58:61], v[168:171], v[176:179], v[58:61]
	v_mfma_i32_16x16x64_i8 v[54:57], v[150:153], v[184:187], v[54:57]
	v_mfma_i32_16x16x64_i8 v[50:53], v[168:171], v[184:187], v[50:53]
	v_mfma_i32_16x16x64_i8 v[46:49], v[150:153], v[192:195], v[46:49]
	v_mfma_i32_16x16x64_i8 v[42:45], v[168:171], v[192:195], v[42:45]
	v_mfma_i32_16x16x64_i8 v[38:41], v[150:153], v[202:205], v[38:41]
	v_mfma_i32_16x16x64_i8 v[34:37], v[168:171], v[202:205], v[34:37]
	s_setprio 0
	s_barrier
	s_add_i32 s68, 0, 0x1c000
	s_add_i32 s69, s90, s4
	v_add_u32_e32 v154, s68, v157
	v_lshl_add_u64 v[222:223], v[222:223], 0, s[28:29]
	s_mov_b32 m0, s69
	ds_read_b128 v[206:209], v154
	ds_read_b128 v[210:213], v154 offset:1024
	ds_read_b128 v[214:217], v154 offset:2048
	ds_read_b128 v[218:221], v154 offset:3072
	global_load_lds_dwordx4 v[222:223], off
	v_lshl_add_u64 v[222:223], v[224:225], 0, s[28:29]
	s_add_i32 m0, s69, 0x2000
	s_nop 0
	global_load_lds_dwordx4 v[222:223], off
	s_barrier
	s_setprio 1
	s_waitcnt lgkmcnt(0)
	v_mfma_i32_16x16x64_i8 v[126:129], v[206:209], v[172:175], v[126:129]
	v_mfma_i32_16x16x64_i8 v[122:125], v[214:217], v[172:175], v[122:125]
	ds_read_b128 v[172:175], v159 offset:49152
	v_mfma_i32_16x16x64_i8 v[118:121], v[206:209], v[180:183], v[118:121]
	v_mfma_i32_16x16x64_i8 v[114:117], v[214:217], v[180:183], v[114:117]
	ds_read_b128 v[180:183], v159 offset:51200
	v_mfma_i32_16x16x64_i8 v[110:113], v[206:209], v[188:191], v[110:113]
	v_mfma_i32_16x16x64_i8 v[106:109], v[214:217], v[188:191], v[106:109]
	ds_read_b128 v[188:191], v159 offset:53248
	v_mfma_i32_16x16x64_i8 v[102:105], v[206:209], v[198:201], v[102:105]
	v_mfma_i32_16x16x64_i8 v[98:101], v[214:217], v[198:201], v[98:101]
	ds_read_b128 v[198:201], v159 offset:55296
	v_mfma_i32_16x16x64_i8 v[126:129], v[210:213], v[176:179], v[126:129]
	v_mfma_i32_16x16x64_i8 v[122:125], v[218:221], v[176:179], v[122:125]
	ds_read_b128 v[176:179], v159 offset:50176
	v_mfma_i32_16x16x64_i8 v[118:121], v[210:213], v[184:187], v[118:121]
	v_mfma_i32_16x16x64_i8 v[114:117], v[218:221], v[184:187], v[114:117]
	ds_read_b128 v[184:187], v159 offset:52224
	v_mfma_i32_16x16x64_i8 v[110:113], v[210:213], v[192:195], v[110:113]
	v_mfma_i32_16x16x64_i8 v[106:109], v[218:221], v[192:195], v[106:109]
	ds_read_b128 v[192:195], v159 offset:54272
	v_mfma_i32_16x16x64_i8 v[102:105], v[210:213], v[202:205], v[102:105]
	v_mfma_i32_16x16x64_i8 v[98:101], v[218:221], v[202:205], v[98:101]
	ds_read_b128 v[202:205], v159 offset:56320
	s_setprio 0
	s_mov_b32 m0, s73
	v_lshl_add_u64 v[222:223], v[226:227], 0, s[28:29]
	s_barrier
	global_load_lds_dwordx4 v[222:223], off
	v_lshl_add_u64 v[222:223], v[228:229], 0, s[28:29]
	s_mov_b32 m0, s74
	s_nop 0
	global_load_lds_dwordx4 v[222:223], off
	s_barrier
	s_setprio 1
	s_waitcnt lgkmcnt(0)
	v_mfma_i32_16x16x64_i8 v[30:33], v[146:149], v[172:175], v[30:33]
	v_mfma_i32_16x16x64_i8 v[26:29], v[164:167], v[172:175], v[26:29]
	v_mfma_i32_16x16x64_i8 v[22:25], v[146:149], v[180:183], v[22:25]
	v_mfma_i32_16x16x64_i8 v[18:21], v[164:167], v[180:183], v[18:21]
	v_mfma_i32_16x16x64_i8 v[14:17], v[146:149], v[188:191], v[14:17]
	v_mfma_i32_16x16x64_i8 v[10:13], v[164:167], v[188:191], v[10:13]
	v_mfma_i32_16x16x64_i8 v[6:9], v[146:149], v[198:201], v[6:9]
	v_mfma_i32_16x16x64_i8 v[2:5], v[164:167], v[198:201], v[2:5]
	v_mfma_i32_16x16x64_i8 v[30:33], v[150:153], v[176:179], v[30:33]
	v_mfma_i32_16x16x64_i8 v[26:29], v[168:171], v[176:179], v[26:29]
	v_mfma_i32_16x16x64_i8 v[22:25], v[150:153], v[184:187], v[22:25]
	v_mfma_i32_16x16x64_i8 v[18:21], v[168:171], v[184:187], v[18:21]
	v_mfma_i32_16x16x64_i8 v[14:17], v[150:153], v[192:195], v[14:17]
	v_mfma_i32_16x16x64_i8 v[10:13], v[168:171], v[192:195], v[10:13]
	v_mfma_i32_16x16x64_i8 v[6:9], v[150:153], v[202:205], v[6:9]
	v_mfma_i32_16x16x64_i8 v[2:5], v[168:171], v[202:205], v[2:5]
	s_setprio 0
	s_barrier
	s_add_u32 s66, s66, 0x40080
	s_addc_u32 s67, s67, 0
	s_add_i32 s68, s68, s4
	v_lshl_add_u64 v[146:147], s[66:67], 0, v[134:135]
	s_mov_b32 m0, s68
	s_nop 0
	global_load_lds_dwordx4 v[146:147], off
	v_lshl_add_u64 v[146:147], s[66:67], 0, v[130:131]
	s_add_i32 m0, s68, 0x2000
	s_nop 0
	global_load_lds_dwordx4 v[146:147], off
	s_waitcnt vmcnt(6)
	s_barrier
	s_setprio 1
	v_mfma_i32_16x16x64_i8 v[94:97], v[206:209], v[172:175], v[94:97]
	v_add_u32_e32 v154, s77, v157
	ds_read_b128 v[146:149], v154
	ds_read_b128 v[150:153], v154 offset:1024
	ds_read_b128 v[164:167], v154 offset:2048
	ds_read_b128 v[168:171], v154 offset:3072
	v_mfma_i32_16x16x64_i8 v[90:93], v[214:217], v[172:175], v[90:93]
	ds_read_b128 v[172:175], v159
	v_mfma_i32_16x16x64_i8 v[86:89], v[206:209], v[180:183], v[86:89]
	v_mfma_i32_16x16x64_i8 v[82:85], v[214:217], v[180:183], v[82:85]
	ds_read_b128 v[180:183], v159 offset:2048
	v_mfma_i32_16x16x64_i8 v[78:81], v[206:209], v[188:191], v[78:81]
	v_mfma_i32_16x16x64_i8 v[74:77], v[214:217], v[188:191], v[74:77]
	ds_read_b128 v[188:191], v159 offset:4096
	v_mfma_i32_16x16x64_i8 v[70:73], v[206:209], v[198:201], v[70:73]
	v_mfma_i32_16x16x64_i8 v[66:69], v[214:217], v[198:201], v[66:69]
	ds_read_b128 v[198:201], v159 offset:6144
	v_mfma_i32_16x16x64_i8 v[94:97], v[210:213], v[176:179], v[94:97]
	v_mfma_i32_16x16x64_i8 v[90:93], v[218:221], v[176:179], v[90:93]
	ds_read_b128 v[176:179], v159 offset:1024
	v_mfma_i32_16x16x64_i8 v[86:89], v[210:213], v[184:187], v[86:89]
	v_mfma_i32_16x16x64_i8 v[82:85], v[218:221], v[184:187], v[82:85]
	ds_read_b128 v[184:187], v159 offset:3072
	v_mfma_i32_16x16x64_i8 v[78:81], v[210:213], v[192:195], v[78:81]
	v_mfma_i32_16x16x64_i8 v[74:77], v[218:221], v[192:195], v[74:77]
	ds_read_b128 v[192:195], v159 offset:5120
	v_mfma_i32_16x16x64_i8 v[70:73], v[210:213], v[202:205], v[70:73]
	v_mfma_i32_16x16x64_i8 v[66:69], v[218:221], v[202:205], v[66:69]
	ds_read_b128 v[202:205], v159 offset:7168
	s_setprio 0
	s_add_u32 s10, s10, 0x100
	s_addc_u32 s11, s11, 0
	s_add_u32 s87, s87, 0x100
	s_addc_u32 s88, s88, 0
	s_cmp_ge_i32 s89, s1
	s_mov_b32 s66, s89
	s_barrier
	s_cbranch_scc0 .LBB0_193
	s_branch .Lmy_pl0_exit
.LBB0_193:
	s_add_i32 s89, s66, 2
	s_add_u32 s67, s10, 0xfffc0080
	s_addc_u32 s68, s11, -1
	s_cmp_eq_u32 s75, s66
	s_cselect_b32 s66, s86, s87
	s_cselect_b32 s69, s9, s68
	s_cselect_b32 s68, s59, s67
	s_cselect_b32 s67, s61, s88
	v_lshl_add_u64 v[206:207], s[10:11], 0, v[138:139]
	s_add_i32 m0, s52, 0xc000
	global_load_lds_dwordx4 v[206:207], off
	v_lshl_add_u64 v[206:207], s[10:11], 0, v[140:141]
	s_add_i32 m0, s52, 0xe000
	s_nop 0
	global_load_lds_dwordx4 v[206:207], off
	s_waitcnt lgkmcnt(8)
	s_barrier
	s_setprio 1
	s_waitcnt lgkmcnt(0)
	v_mfma_i32_16x16x64_i8 v[62:65], v[146:149], v[172:175], v[62:65]
	v_mfma_i32_16x16x64_i8 v[58:61], v[164:167], v[172:175], v[58:61]
	v_mfma_i32_16x16x64_i8 v[54:57], v[146:149], v[180:183], v[54:57]
	v_mfma_i32_16x16x64_i8 v[50:53], v[164:167], v[180:183], v[50:53]
	v_mfma_i32_16x16x64_i8 v[46:49], v[146:149], v[188:191], v[46:49]
	v_mfma_i32_16x16x64_i8 v[42:45], v[164:167], v[188:191], v[42:45]
	v_mfma_i32_16x16x64_i8 v[38:41], v[146:149], v[198:201], v[38:41]
	v_mfma_i32_16x16x64_i8 v[34:37], v[164:167], v[198:201], v[34:37]
	v_mfma_i32_16x16x64_i8 v[62:65], v[150:153], v[176:179], v[62:65]
	v_mfma_i32_16x16x64_i8 v[58:61], v[168:171], v[176:179], v[58:61]
	v_mfma_i32_16x16x64_i8 v[54:57], v[150:153], v[184:187], v[54:57]
	v_mfma_i32_16x16x64_i8 v[50:53], v[168:171], v[184:187], v[50:53]
	v_mfma_i32_16x16x64_i8 v[46:49], v[150:153], v[192:195], v[46:49]
	v_mfma_i32_16x16x64_i8 v[42:45], v[168:171], v[192:195], v[42:45]
	v_mfma_i32_16x16x64_i8 v[38:41], v[150:153], v[202:205], v[38:41]
	v_mfma_i32_16x16x64_i8 v[34:37], v[168:171], v[202:205], v[34:37]
	s_setprio 0
	s_barrier
	s_add_i32 s90, s77, s4
	v_add_u32_e32 v154, s78, v157
	v_lshl_add_u64 v[222:223], s[66:67], 0, v[134:135]
	s_mov_b32 m0, s90
	ds_read_b128 v[206:209], v154
	ds_read_b128 v[210:213], v154 offset:1024
	ds_read_b128 v[214:217], v154 offset:2048
	ds_read_b128 v[218:221], v154 offset:3072
	global_load_lds_dwordx4 v[222:223], off
	v_lshl_add_u64 v[224:225], s[66:67], 0, v[130:131]
	s_add_i32 m0, s90, 0x2000
	s_nop 0
	global_load_lds_dwordx4 v[224:225], off
	s_barrier
	s_setprio 1
	s_waitcnt lgkmcnt(0)
	v_mfma_i32_16x16x64_i8 v[126:129], v[206:209], v[172:175], v[126:129]
	v_mfma_i32_16x16x64_i8 v[122:125], v[214:217], v[172:175], v[122:125]
	ds_read_b128 v[172:175], v159 offset:16384
	v_mfma_i32_16x16x64_i8 v[118:121], v[206:209], v[180:183], v[118:121]
	v_mfma_i32_16x16x64_i8 v[114:117], v[214:217], v[180:183], v[114:117]
	ds_read_b128 v[180:183], v159 offset:18432
	v_mfma_i32_16x16x64_i8 v[110:113], v[206:209], v[188:191], v[110:113]
	v_mfma_i32_16x16x64_i8 v[106:109], v[214:217], v[188:191], v[106:109]
	ds_read_b128 v[188:191], v159 offset:20480
	v_mfma_i32_16x16x64_i8 v[102:105], v[206:209], v[198:201], v[102:105]
	v_mfma_i32_16x16x64_i8 v[98:101], v[214:217], v[198:201], v[98:101]
	ds_read_b128 v[198:201], v159 offset:22528
	v_mfma_i32_16x16x64_i8 v[126:129], v[210:213], v[176:179], v[126:129]
	v_mfma_i32_16x16x64_i8 v[122:125], v[218:221], v[176:179], v[122:125]
	ds_read_b128 v[176:179], v159 offset:17408
	v_mfma_i32_16x16x64_i8 v[118:121], v[210:213], v[184:187], v[118:121]
	v_mfma_i32_16x16x64_i8 v[114:117], v[218:221], v[184:187], v[114:117]
	ds_read_b128 v[184:187], v159 offset:19456
	v_mfma_i32_16x16x64_i8 v[110:113], v[210:213], v[192:195], v[110:113]
	v_mfma_i32_16x16x64_i8 v[106:109], v[218:221], v[192:195], v[106:109]
	ds_read_b128 v[192:195], v159 offset:21504
	v_mfma_i32_16x16x64_i8 v[102:105], v[210:213], v[202:205], v[102:105]
	v_mfma_i32_16x16x64_i8 v[98:101], v[218:221], v[202:205], v[98:101]
	ds_read_b128 v[202:205], v159 offset:23552
	s_setprio 0
	s_mov_b32 m0, s52
	v_lshl_add_u64 v[226:227], s[68:69], 0, v[136:137]
	s_barrier
	global_load_lds_dwordx4 v[226:227], off
	v_lshl_add_u64 v[228:229], s[68:69], 0, v[132:133]
	s_mov_b32 m0, s53
	s_nop 0
	global_load_lds_dwordx4 v[228:229], off
	s_barrier
	s_setprio 1
	s_waitcnt lgkmcnt(0)
	v_mfma_i32_16x16x64_i8 v[30:33], v[146:149], v[172:175], v[30:33]
	v_mfma_i32_16x16x64_i8 v[26:29], v[164:167], v[172:175], v[26:29]
	v_mfma_i32_16x16x64_i8 v[22:25], v[146:149], v[180:183], v[22:25]
	v_mfma_i32_16x16x64_i8 v[18:21], v[164:167], v[180:183], v[18:21]
	v_mfma_i32_16x16x64_i8 v[14:17], v[146:149], v[188:191], v[14:17]
	v_mfma_i32_16x16x64_i8 v[10:13], v[164:167], v[188:191], v[10:13]
	v_mfma_i32_16x16x64_i8 v[6:9], v[146:149], v[198:201], v[6:9]
	v_mfma_i32_16x16x64_i8 v[2:5], v[164:167], v[198:201], v[2:5]
	v_mfma_i32_16x16x64_i8 v[30:33], v[150:153], v[176:179], v[30:33]
	v_mfma_i32_16x16x64_i8 v[26:29], v[168:171], v[176:179], v[26:29]
	v_mfma_i32_16x16x64_i8 v[22:25], v[150:153], v[184:187], v[22:25]
	v_mfma_i32_16x16x64_i8 v[18:21], v[168:171], v[184:187], v[18:21]
	v_mfma_i32_16x16x64_i8 v[14:17], v[150:153], v[192:195], v[14:17]
	v_mfma_i32_16x16x64_i8 v[10:13], v[168:171], v[192:195], v[10:13]
	v_mfma_i32_16x16x64_i8 v[6:9], v[150:153], v[202:205], v[6:9]
	v_mfma_i32_16x16x64_i8 v[2:5], v[168:171], v[202:205], v[2:5]
	s_setprio 0
	s_barrier
	s_add_u32 s90, s66, 0x40000
	s_addc_u32 s91, s67, 0
	s_add_i32 s92, s78, s4
	v_lshl_add_u64 v[146:147], s[90:91], 0, v[134:135]
	s_mov_b32 m0, s92
	s_nop 0
	global_load_lds_dwordx4 v[146:147], off
	v_lshl_add_u64 v[146:147], s[90:91], 0, v[130:131]
	s_add_i32 m0, s92, 0x2000
	s_nop 0
	global_load_lds_dwordx4 v[146:147], off
	s_waitcnt vmcnt(6)
	s_barrier
	s_setprio 1
	v_mfma_i32_16x16x64_i8 v[94:97], v[206:209], v[172:175], v[94:97]
	v_mfma_i32_16x16x64_i8 v[90:93], v[214:217], v[172:175], v[90:93]
	ds_read_b128 v[172:175], v159 offset:32768
	v_mfma_i32_16x16x64_i8 v[86:89], v[206:209], v[180:183], v[86:89]
	v_mfma_i32_16x16x64_i8 v[82:85], v[214:217], v[180:183], v[82:85]
	ds_read_b128 v[180:183], v159 offset:34816
	v_mfma_i32_16x16x64_i8 v[78:81], v[206:209], v[188:191], v[78:81]
	v_mfma_i32_16x16x64_i8 v[74:77], v[214:217], v[188:191], v[74:77]
	ds_read_b128 v[188:191], v159 offset:36864
	v_mfma_i32_16x16x64_i8 v[70:73], v[206:209], v[198:201], v[70:73]
	v_mfma_i32_16x16x64_i8 v[66:69], v[214:217], v[198:201], v[66:69]
	ds_read_b128 v[198:201], v159 offset:38912
	v_mfma_i32_16x16x64_i8 v[94:97], v[210:213], v[176:179], v[94:97]
	v_mfma_i32_16x16x64_i8 v[90:93], v[218:221], v[176:179], v[90:93]
	ds_read_b128 v[176:179], v159 offset:33792
	v_mfma_i32_16x16x64_i8 v[86:89], v[210:213], v[184:187], v[86:89]
	v_mfma_i32_16x16x64_i8 v[82:85], v[218:221], v[184:187], v[82:85]
	ds_read_b128 v[184:187], v159 offset:35840
	v_mfma_i32_16x16x64_i8 v[78:81], v[210:213], v[192:195], v[78:81]
	v_mfma_i32_16x16x64_i8 v[74:77], v[218:221], v[192:195], v[74:77]
	ds_read_b128 v[192:195], v159 offset:37888
	v_mfma_i32_16x16x64_i8 v[70:73], v[210:213], v[202:205], v[70:73]
	v_mfma_i32_16x16x64_i8 v[66:69], v[218:221], v[202:205], v[66:69]
	ds_read_b128 v[202:205], v159 offset:39936
	s_setprio 0
	s_add_i32 s90, 0, 0x18000
	v_add_u32_e32 v154, s90, v157
	s_barrier
	ds_read_b128 v[146:149], v154
	ds_read_b128 v[150:153], v154 offset:1024
	ds_read_b128 v[164:167], v154 offset:2048
	ds_read_b128 v[168:171], v154 offset:3072
	s_add_u32 s68, s68, 0x40000
	s_addc_u32 s69, s69, 0
	s_mov_b32 m0, s54
	v_lshl_add_u64 v[206:207], s[68:69], 0, v[136:137]
	global_load_lds_dwordx4 v[206:207], off
	v_lshl_add_u64 v[206:207], s[68:69], 0, v[132:133]
	s_mov_b32 m0, s55
	s_nop 0
	global_load_lds_dwordx4 v[206:207], off
	s_waitcnt lgkmcnt(8)
	s_barrier
	s_setprio 1
	s_waitcnt lgkmcnt(0)
	v_mfma_i32_16x16x64_i8 v[62:65], v[146:149], v[172:175], v[62:65]
	v_mfma_i32_16x16x64_i8 v[58:61], v[164:167], v[172:175], v[58:61]
	v_mfma_i32_16x16x64_i8 v[54:57], v[146:149], v[180:183], v[54:57]
	v_mfma_i32_16x16x64_i8 v[50:53], v[164:167], v[180:183], v[50:53]
	v_mfma_i32_16x16x64_i8 v[46:49], v[146:149], v[188:191], v[46:49]
	v_mfma_i32_16x16x64_i8 v[42:45], v[164:167], v[188:191], v[42:45]
	v_mfma_i32_16x16x64_i8 v[38:41], v[146:149], v[198:201], v[38:41]
	v_mfma_i32_16x16x64_i8 v[34:37], v[164:167], v[198:201], v[34:37]
	v_mfma_i32_16x16x64_i8 v[62:65], v[150:153], v[176:179], v[62:65]
	v_mfma_i32_16x16x64_i8 v[58:61], v[168:171], v[176:179], v[58:61]
	v_mfma_i32_16x16x64_i8 v[54:57], v[150:153], v[184:187], v[54:57]
	v_mfma_i32_16x16x64_i8 v[50:53], v[168:171], v[184:187], v[50:53]
	v_mfma_i32_16x16x64_i8 v[46:49], v[150:153], v[192:195], v[46:49]
	v_mfma_i32_16x16x64_i8 v[42:45], v[168:171], v[192:195], v[42:45]
	v_mfma_i32_16x16x64_i8 v[38:41], v[150:153], v[202:205], v[38:41]
	v_mfma_i32_16x16x64_i8 v[34:37], v[168:171], v[202:205], v[34:37]
	s_setprio 0
	s_barrier
	s_add_i32 s68, 0, 0x1c000
	s_add_i32 s69, s90, s4
	v_add_u32_e32 v154, s68, v157
	v_lshl_add_u64 v[222:223], v[222:223], 0, s[28:29]
	s_mov_b32 m0, s69
	ds_read_b128 v[206:209], v154
	ds_read_b128 v[210:213], v154 offset:1024
	ds_read_b128 v[214:217], v154 offset:2048
	ds_read_b128 v[218:221], v154 offset:3072
	global_load_lds_dwordx4 v[222:223], off
	v_lshl_add_u64 v[222:223], v[224:225], 0, s[28:29]
	s_add_i32 m0, s69, 0x2000
	s_nop 0
	global_load_lds_dwordx4 v[222:223], off
	s_barrier
	s_setprio 1
	s_waitcnt lgkmcnt(0)
	v_mfma_i32_16x16x64_i8 v[126:129], v[206:209], v[172:175], v[126:129]
	v_mfma_i32_16x16x64_i8 v[122:125], v[214:217], v[172:175], v[122:125]
	ds_read_b128 v[172:175], v159 offset:49152
	v_mfma_i32_16x16x64_i8 v[118:121], v[206:209], v[180:183], v[118:121]
	v_mfma_i32_16x16x64_i8 v[114:117], v[214:217], v[180:183], v[114:117]
	ds_read_b128 v[180:183], v159 offset:51200
	v_mfma_i32_16x16x64_i8 v[110:113], v[206:209], v[188:191], v[110:113]
	v_mfma_i32_16x16x64_i8 v[106:109], v[214:217], v[188:191], v[106:109]
	ds_read_b128 v[188:191], v159 offset:53248
	v_mfma_i32_16x16x64_i8 v[102:105], v[206:209], v[198:201], v[102:105]
	v_mfma_i32_16x16x64_i8 v[98:101], v[214:217], v[198:201], v[98:101]
	ds_read_b128 v[198:201], v159 offset:55296
	v_mfma_i32_16x16x64_i8 v[126:129], v[210:213], v[176:179], v[126:129]
	v_mfma_i32_16x16x64_i8 v[122:125], v[218:221], v[176:179], v[122:125]
	ds_read_b128 v[176:179], v159 offset:50176
	v_mfma_i32_16x16x64_i8 v[118:121], v[210:213], v[184:187], v[118:121]
	v_mfma_i32_16x16x64_i8 v[114:117], v[218:221], v[184:187], v[114:117]
	ds_read_b128 v[184:187], v159 offset:52224
	v_mfma_i32_16x16x64_i8 v[110:113], v[210:213], v[192:195], v[110:113]
	v_mfma_i32_16x16x64_i8 v[106:109], v[218:221], v[192:195], v[106:109]
	ds_read_b128 v[192:195], v159 offset:54272
	v_mfma_i32_16x16x64_i8 v[102:105], v[210:213], v[202:205], v[102:105]
	v_mfma_i32_16x16x64_i8 v[98:101], v[218:221], v[202:205], v[98:101]
	ds_read_b128 v[202:205], v159 offset:56320
	s_setprio 0
	s_mov_b32 m0, s73
	v_lshl_add_u64 v[222:223], v[226:227], 0, s[28:29]
	s_barrier
	global_load_lds_dwordx4 v[222:223], off
	v_lshl_add_u64 v[222:223], v[228:229], 0, s[28:29]
	s_mov_b32 m0, s74
	s_nop 0
	global_load_lds_dwordx4 v[222:223], off
	s_barrier
	s_setprio 1
	s_waitcnt lgkmcnt(0)
	v_mfma_i32_16x16x64_i8 v[30:33], v[146:149], v[172:175], v[30:33]
	v_mfma_i32_16x16x64_i8 v[26:29], v[164:167], v[172:175], v[26:29]
	v_mfma_i32_16x16x64_i8 v[22:25], v[146:149], v[180:183], v[22:25]
	v_mfma_i32_16x16x64_i8 v[18:21], v[164:167], v[180:183], v[18:21]
	v_mfma_i32_16x16x64_i8 v[14:17], v[146:149], v[188:191], v[14:17]
	v_mfma_i32_16x16x64_i8 v[10:13], v[164:167], v[188:191], v[10:13]
	v_mfma_i32_16x16x64_i8 v[6:9], v[146:149], v[198:201], v[6:9]
	v_mfma_i32_16x16x64_i8 v[2:5], v[164:167], v[198:201], v[2:5]
	v_mfma_i32_16x16x64_i8 v[30:33], v[150:153], v[176:179], v[30:33]
	v_mfma_i32_16x16x64_i8 v[26:29], v[168:171], v[176:179], v[26:29]
	v_mfma_i32_16x16x64_i8 v[22:25], v[150:153], v[184:187], v[22:25]
	v_mfma_i32_16x16x64_i8 v[18:21], v[168:171], v[184:187], v[18:21]
	v_mfma_i32_16x16x64_i8 v[14:17], v[150:153], v[192:195], v[14:17]
	v_mfma_i32_16x16x64_i8 v[10:13], v[168:171], v[192:195], v[10:13]
	v_mfma_i32_16x16x64_i8 v[6:9], v[150:153], v[202:205], v[6:9]
	v_mfma_i32_16x16x64_i8 v[2:5], v[168:171], v[202:205], v[2:5]
	s_setprio 0
	s_barrier
	s_add_u32 s66, s66, 0x40080
	s_addc_u32 s67, s67, 0
	s_add_i32 s68, s68, s4
	v_lshl_add_u64 v[146:147], s[66:67], 0, v[134:135]
	s_mov_b32 m0, s68
	s_nop 0
	global_load_lds_dwordx4 v[146:147], off
	v_lshl_add_u64 v[146:147], s[66:67], 0, v[130:131]
	s_add_i32 m0, s68, 0x2000
	s_nop 0
	global_load_lds_dwordx4 v[146:147], off
	s_waitcnt vmcnt(6)
	s_barrier
	s_setprio 1
	v_mfma_i32_16x16x64_i8 v[94:97], v[206:209], v[172:175], v[94:97]
	v_add_u32_e32 v154, s77, v157
	ds_read_b128 v[146:149], v154
	ds_read_b128 v[150:153], v154 offset:1024
	ds_read_b128 v[164:167], v154 offset:2048
	ds_read_b128 v[168:171], v154 offset:3072
	v_mfma_i32_16x16x64_i8 v[90:93], v[214:217], v[172:175], v[90:93]
	ds_read_b128 v[172:175], v159
	v_mfma_i32_16x16x64_i8 v[86:89], v[206:209], v[180:183], v[86:89]
	v_mfma_i32_16x16x64_i8 v[82:85], v[214:217], v[180:183], v[82:85]
	ds_read_b128 v[180:183], v159 offset:2048
	v_mfma_i32_16x16x64_i8 v[78:81], v[206:209], v[188:191], v[78:81]
	v_mfma_i32_16x16x64_i8 v[74:77], v[214:217], v[188:191], v[74:77]
	ds_read_b128 v[188:191], v159 offset:4096
	v_mfma_i32_16x16x64_i8 v[70:73], v[206:209], v[198:201], v[70:73]
	v_mfma_i32_16x16x64_i8 v[66:69], v[214:217], v[198:201], v[66:69]
	ds_read_b128 v[198:201], v159 offset:6144
	v_mfma_i32_16x16x64_i8 v[94:97], v[210:213], v[176:179], v[94:97]
	v_mfma_i32_16x16x64_i8 v[90:93], v[218:221], v[176:179], v[90:93]
	ds_read_b128 v[176:179], v159 offset:1024
	v_mfma_i32_16x16x64_i8 v[86:89], v[210:213], v[184:187], v[86:89]
	v_mfma_i32_16x16x64_i8 v[82:85], v[218:221], v[184:187], v[82:85]
	ds_read_b128 v[184:187], v159 offset:3072
	v_mfma_i32_16x16x64_i8 v[78:81], v[210:213], v[192:195], v[78:81]
	v_mfma_i32_16x16x64_i8 v[74:77], v[218:221], v[192:195], v[74:77]
	ds_read_b128 v[192:195], v159 offset:5120
	v_mfma_i32_16x16x64_i8 v[70:73], v[210:213], v[202:205], v[70:73]
	v_mfma_i32_16x16x64_i8 v[66:69], v[218:221], v[202:205], v[66:69]
	ds_read_b128 v[202:205], v159 offset:7168
	s_setprio 0
	s_add_u32 s10, s10, 0x100
	s_addc_u32 s11, s11, 0
	s_add_u32 s87, s87, 0x100
	s_addc_u32 s88, s88, 0
	s_cmp_ge_i32 s89, s1
	s_mov_b32 s66, s89
	s_barrier
	s_cbranch_scc0 .LBB0_193
.Lmy_pl0_exit:
	s_waitcnt lgkmcnt(0)
	v_cvt_f32_i32_e32 v150, v126
	v_cvt_f32_i32_e32 v151, v127
	v_cvt_f32_i32_e32 v126, v128
	v_cvt_f32_i32_e32 v127, v129
	v_cvt_f32_i32_e32 v148, v122
	v_cvt_f32_i32_e32 v149, v123
	v_cvt_f32_i32_e32 v152, v124
	v_cvt_f32_i32_e32 v153, v125
	v_cvt_f32_i32_e32 v124, v118
	v_cvt_f32_i32_e32 v125, v119
	v_cvt_f32_i32_e32 v146, v120
	v_cvt_f32_i32_e32 v147, v121
	v_cvt_f32_i32_e32 v122, v114
	v_cvt_f32_i32_e32 v123, v115
	v_cvt_f32_i32_e32 v128, v116
	v_cvt_f32_i32_e32 v129, v117
	v_cvt_f32_i32_e32 v114, v110
	v_cvt_f32_i32_e32 v115, v111
	v_cvt_f32_i32_e32 v120, v112
	v_cvt_f32_i32_e32 v121, v113
	v_cvt_f32_i32_e32 v110, v106
	v_cvt_f32_i32_e32 v111, v107
	v_cvt_f32_i32_e32 v118, v108
	v_cvt_f32_i32_e32 v119, v109
	v_cvt_f32_i32_e32 v102, v102
	v_cvt_f32_i32_e32 v103, v103
	v_cvt_f32_i32_e32 v104, v104
	v_cvt_f32_i32_e32 v105, v105
	v_cvt_f32_i32_e32 v98, v98
	v_cvt_f32_i32_e32 v99, v99
	v_cvt_f32_i32_e32 v100, v100
	v_cvt_f32_i32_e32 v101, v101
	v_cvt_f32_i32_e32 v108, v94
	v_cvt_f32_i32_e32 v109, v95
	v_cvt_f32_i32_e32 v116, v96
	v_cvt_f32_i32_e32 v117, v97
	v_cvt_f32_i32_e32 v106, v90
	v_cvt_f32_i32_e32 v107, v91
	v_cvt_f32_i32_e32 v112, v92
	v_cvt_f32_i32_e32 v113, v93
	v_cvt_f32_i32_e32 v92, v86
	v_cvt_f32_i32_e32 v93, v87
	v_cvt_f32_i32_e32 v96, v88
	v_cvt_f32_i32_e32 v97, v89
	v_cvt_f32_i32_e32 v90, v82
	v_cvt_f32_i32_e32 v91, v83
	v_cvt_f32_i32_e32 v94, v84
	v_cvt_f32_i32_e32 v95, v85
	v_cvt_f32_i32_e32 v84, v78
	v_cvt_f32_i32_e32 v85, v79
	v_cvt_f32_i32_e32 v88, v80
	v_cvt_f32_i32_e32 v89, v81
	v_cvt_f32_i32_e32 v82, v74
	v_cvt_f32_i32_e32 v83, v75
	v_cvt_f32_i32_e32 v86, v76
	v_cvt_f32_i32_e32 v87, v77
	v_cvt_f32_i32_e32 v76, v70
	v_cvt_f32_i32_e32 v77, v71
	v_cvt_f32_i32_e32 v80, v72
	v_cvt_f32_i32_e32 v81, v73
	v_cvt_f32_i32_e32 v74, v66
	v_cvt_f32_i32_e32 v75, v67
	v_cvt_f32_i32_e32 v78, v68
	v_cvt_f32_i32_e32 v79, v69
	s_branch .LBB0_196

.LBB0_962:
	s_ashr_i32 s27, s26, 31
	s_lshl_b64 s[28:29], s[26:27], 20
	s_add_u32 s28, s10, s28
	s_addc_u32 s29, s11, s29
	s_ashr_i32 s25, s24, 31
	s_lshl_b64 s[30:31], s[24:25], 20
	s_add_u32 s30, s14, s30
	v_cmp_lt_i64_e64 s[8:9], s[8:9], v[158:159]
	s_addc_u32 s31, s15, s31
	s_andn2_b64 vcc, exec, s[20:21]
	s_cbranch_vccnz .LBB0_954
	s_and_b64 s[8:9], s[8:9], exec
	s_cselect_b32 s25, s29, s39
	s_cselect_b32 s27, s28, s38
	s_cselect_b32 s51, s31, s37
	s_cselect_b32 s52, s30, s36
	s_add_u32 s8, s38, 0x80080
	s_addc_u32 s9, s39, 0
	s_add_u32 s53, s36, 0x100
	v_mov_b32_e32 v2, 0
	s_addc_u32 s54, s37, 0
	s_mov_b32 s36, 0
	ds_read_b128 v[130:133], v172
	ds_read_b128 v[134:137], v172 offset:1024
	ds_read_b128 v[138:141], v172 offset:2048
	ds_read_b128 v[142:145], v172 offset:3072
	s_add_i32 s55, s36, 2
	s_add_u32 s37, s8, 0xfff80080
	s_addc_u32 s38, s9, -1
	s_cmp_eq_u32 s46, s36
	s_cselect_b32 s36, s52, s53
	s_cselect_b32 s39, s25, s38
	s_cselect_b32 s38, s27, s37
	s_cselect_b32 s37, s51, s54
	v_lshl_add_u64 v[200:201], s[8:9], 0, v[154:155]
	s_add_i32 m0, s23, 0xc000
	ds_read_b128 v[162:165], v173
	ds_read_b128 v[166:169], v173 offset:1024
	ds_read_b128 v[176:179], v173 offset:2048
	ds_read_b128 v[180:183], v173 offset:3072
	ds_read_b128 v[184:187], v173 offset:4096
	ds_read_b128 v[188:191], v173 offset:5120
	ds_read_b128 v[192:195], v173 offset:6144
	ds_read_b128 v[196:199], v173 offset:7168
	global_load_lds_dwordx4 v[200:201], off
	v_lshl_add_u64 v[200:201], s[8:9], 0, v[156:157]
	s_add_i32 m0, s23, 0xe000
	s_nop 0
	global_load_lds_dwordx4 v[200:201], off
	s_waitcnt lgkmcnt(8)
	s_barrier
	s_setprio 1
	s_waitcnt lgkmcnt(0)
	v_mfma_f32_16x16x32_bf16 v[126:129], v[130:133], v[162:165], 0
	ds_read_b128 v[200:203], v174
	ds_read_b128 v[204:207], v174 offset:1024
	ds_read_b128 v[208:211], v174 offset:2048
	ds_read_b128 v[214:217], v174 offset:3072
	v_mfma_f32_16x16x32_bf16 v[122:125], v[138:141], v[162:165], 0
	v_mfma_f32_16x16x32_bf16 v[110:113], v[130:133], v[176:179], 0
	v_mfma_f32_16x16x32_bf16 v[106:109], v[138:141], v[176:179], 0
	v_mfma_f32_16x16x32_bf16 v[94:97], v[130:133], v[184:187], 0
	v_mfma_f32_16x16x32_bf16 v[90:93], v[138:141], v[184:187], 0
	v_mfma_f32_16x16x32_bf16 v[78:81], v[130:133], v[192:195], 0
	v_mfma_f32_16x16x32_bf16 v[74:77], v[138:141], v[192:195], 0
	v_mfma_f32_16x16x32_bf16 v[126:129], v[134:137], v[166:169], v[126:129]
	v_mfma_f32_16x16x32_bf16 v[122:125], v[142:145], v[166:169], v[122:125]
	v_mfma_f32_16x16x32_bf16 v[110:113], v[134:137], v[180:183], v[110:113]
	v_mfma_f32_16x16x32_bf16 v[106:109], v[142:145], v[180:183], v[106:109]
	v_mfma_f32_16x16x32_bf16 v[94:97], v[134:137], v[188:191], v[94:97]
	v_mfma_f32_16x16x32_bf16 v[90:93], v[142:145], v[188:191], v[90:93]
	v_mfma_f32_16x16x32_bf16 v[78:81], v[134:137], v[196:199], v[78:81]
	v_mfma_f32_16x16x32_bf16 v[74:77], v[142:145], v[196:199], v[74:77]
	s_setprio 0
	s_barrier
	s_add_i32 s56, s48, s5
	v_lshl_add_u64 v[218:219], s[36:37], 0, v[148:149]
	s_mov_b32 m0, s56
	global_load_lds_dwordx4 v[218:219], off
	v_lshl_add_u64 v[220:221], s[36:37], 0, v[152:153]
	s_add_i32 m0, s56, 0x2000
	s_nop 0
	global_load_lds_dwordx4 v[220:221], off
	s_barrier
	s_setprio 1
	s_waitcnt lgkmcnt(0)
	v_mfma_f32_16x16x32_bf16 v[118:121], v[200:203], v[162:165], 0
	v_mfma_f32_16x16x32_bf16 v[114:117], v[208:211], v[162:165], 0
	ds_read_b128 v[162:165], v173 offset:16384
	v_mfma_f32_16x16x32_bf16 v[102:105], v[200:203], v[176:179], 0
	v_mfma_f32_16x16x32_bf16 v[98:101], v[208:211], v[176:179], 0
	ds_read_b128 v[176:179], v173 offset:18432
	v_mfma_f32_16x16x32_bf16 v[86:89], v[200:203], v[184:187], 0
	v_mfma_f32_16x16x32_bf16 v[82:85], v[208:211], v[184:187], 0
	ds_read_b128 v[184:187], v173 offset:20480
	v_mfma_f32_16x16x32_bf16 v[70:73], v[200:203], v[192:195], 0
	v_mfma_f32_16x16x32_bf16 v[66:69], v[208:211], v[192:195], 0
	ds_read_b128 v[192:195], v173 offset:22528
	v_mfma_f32_16x16x32_bf16 v[118:121], v[204:207], v[166:169], v[118:121]
	v_mfma_f32_16x16x32_bf16 v[114:117], v[214:217], v[166:169], v[114:117]
	ds_read_b128 v[166:169], v173 offset:17408
	v_mfma_f32_16x16x32_bf16 v[102:105], v[204:207], v[180:183], v[102:105]
	v_mfma_f32_16x16x32_bf16 v[98:101], v[214:217], v[180:183], v[98:101]
	ds_read_b128 v[180:183], v173 offset:19456
	v_mfma_f32_16x16x32_bf16 v[86:89], v[204:207], v[188:191], v[86:89]
	v_mfma_f32_16x16x32_bf16 v[82:85], v[214:217], v[188:191], v[82:85]
	ds_read_b128 v[188:191], v173 offset:21504
	v_mfma_f32_16x16x32_bf16 v[70:73], v[204:207], v[196:199], v[70:73]
	v_mfma_f32_16x16x32_bf16 v[66:69], v[214:217], v[196:199], v[66:69]
	ds_read_b128 v[196:199], v173 offset:23552
	s_setprio 0
	s_mov_b32 m0, s23
	v_lshl_add_u64 v[222:223], s[38:39], 0, v[146:147]
	s_barrier
	global_load_lds_dwordx4 v[222:223], off
	v_lshl_add_u64 v[224:225], s[38:39], 0, v[150:151]
	s_mov_b32 m0, s33
	s_nop 0
	global_load_lds_dwordx4 v[224:225], off
	s_barrier
	s_setprio 1
	s_waitcnt lgkmcnt(0)
	v_mfma_f32_16x16x32_bf16 v[62:65], v[130:133], v[162:165], 0
	v_mfma_f32_16x16x32_bf16 v[58:61], v[138:141], v[162:165], 0
	v_mfma_f32_16x16x32_bf16 v[46:49], v[130:133], v[176:179], 0
	v_mfma_f32_16x16x32_bf16 v[42:45], v[138:141], v[176:179], 0
	v_mfma_f32_16x16x32_bf16 v[30:33], v[130:133], v[184:187], 0
	v_mfma_f32_16x16x32_bf16 v[26:29], v[138:141], v[184:187], 0
	v_mfma_f32_16x16x32_bf16 v[14:17], v[130:133], v[192:195], 0
	v_mfma_f32_16x16x32_bf16 v[10:13], v[138:141], v[192:195], 0
	v_mfma_f32_16x16x32_bf16 v[62:65], v[134:137], v[166:169], v[62:65]
	v_mfma_f32_16x16x32_bf16 v[58:61], v[142:145], v[166:169], v[58:61]
	v_mfma_f32_16x16x32_bf16 v[46:49], v[134:137], v[180:183], v[46:49]
	v_mfma_f32_16x16x32_bf16 v[42:45], v[142:145], v[180:183], v[42:45]
	v_mfma_f32_16x16x32_bf16 v[30:33], v[134:137], v[188:191], v[30:33]
	v_mfma_f32_16x16x32_bf16 v[26:29], v[142:145], v[188:191], v[26:29]
	v_mfma_f32_16x16x32_bf16 v[14:17], v[134:137], v[196:199], v[14:17]
	v_mfma_f32_16x16x32_bf16 v[10:13], v[142:145], v[196:199], v[10:13]
	s_setprio 0
	s_barrier
	s_add_u32 s56, s36, 0x80000
	s_addc_u32 s57, s37, 0
	s_add_i32 s58, s49, s5
	v_lshl_add_u64 v[130:131], s[56:57], 0, v[148:149]
	s_mov_b32 m0, s58
	s_nop 0
	global_load_lds_dwordx4 v[130:131], off
	v_lshl_add_u64 v[130:131], s[56:57], 0, v[152:153]
	s_add_i32 m0, s58, 0x2000
	s_nop 0
	global_load_lds_dwordx4 v[130:131], off
	s_waitcnt vmcnt(6)
	s_barrier
	s_setprio 1
	v_mfma_f32_16x16x32_bf16 v[54:57], v[200:203], v[162:165], 0
	v_mfma_f32_16x16x32_bf16 v[50:53], v[208:211], v[162:165], 0
	ds_read_b128 v[162:165], v173 offset:32768
	v_mfma_f32_16x16x32_bf16 v[38:41], v[200:203], v[176:179], 0
	v_mfma_f32_16x16x32_bf16 v[34:37], v[208:211], v[176:179], 0
	ds_read_b128 v[176:179], v173 offset:34816
	v_mfma_f32_16x16x32_bf16 v[22:25], v[200:203], v[184:187], 0
	v_mfma_f32_16x16x32_bf16 v[18:21], v[208:211], v[184:187], 0
	ds_read_b128 v[184:187], v173 offset:36864
	v_mfma_f32_16x16x32_bf16 v[6:9], v[200:203], v[192:195], 0
	v_mfma_f32_16x16x32_bf16 v[2:5], v[208:211], v[192:195], 0
	ds_read_b128 v[192:195], v173 offset:38912
	v_mfma_f32_16x16x32_bf16 v[54:57], v[204:207], v[166:169], v[54:57]
	v_mfma_f32_16x16x32_bf16 v[50:53], v[214:217], v[166:169], v[50:53]
	ds_read_b128 v[166:169], v173 offset:33792
	v_mfma_f32_16x16x32_bf16 v[38:41], v[204:207], v[180:183], v[38:41]
	v_mfma_f32_16x16x32_bf16 v[34:37], v[214:217], v[180:183], v[34:37]
	ds_read_b128 v[180:183], v173 offset:35840
	v_mfma_f32_16x16x32_bf16 v[22:25], v[204:207], v[188:191], v[22:25]
	v_mfma_f32_16x16x32_bf16 v[18:21], v[214:217], v[188:191], v[18:21]
	ds_read_b128 v[188:191], v173 offset:37888
	v_mfma_f32_16x16x32_bf16 v[6:9], v[204:207], v[196:199], v[6:9]
	v_mfma_f32_16x16x32_bf16 v[2:5], v[214:217], v[196:199], v[2:5]
	ds_read_b128 v[196:199], v173 offset:39936
	s_setprio 0
	s_add_i32 s56, 0, 0x18000
	v_add_u32_e32 v142, s56, v171
	s_barrier
	ds_read_b128 v[130:133], v142
	ds_read_b128 v[134:137], v142 offset:1024
	ds_read_b128 v[138:141], v142 offset:2048
	ds_read_b128 v[142:145], v142 offset:3072
	s_add_u32 s38, s38, 0x80000
	s_addc_u32 s39, s39, 0
	s_mov_b32 m0, s35
	v_lshl_add_u64 v[200:201], s[38:39], 0, v[146:147]
	global_load_lds_dwordx4 v[200:201], off
	v_lshl_add_u64 v[200:201], s[38:39], 0, v[150:151]
	s_mov_b32 m0, s40
	s_nop 0
	global_load_lds_dwordx4 v[200:201], off
	s_waitcnt lgkmcnt(8)
	s_barrier
	s_setprio 1
	s_waitcnt lgkmcnt(0)
	v_mfma_f32_16x16x32_bf16 v[126:129], v[130:133], v[162:165], v[126:129]
	v_mfma_f32_16x16x32_bf16 v[122:125], v[138:141], v[162:165], v[122:125]
	v_mfma_f32_16x16x32_bf16 v[110:113], v[130:133], v[176:179], v[110:113]
	v_mfma_f32_16x16x32_bf16 v[106:109], v[138:141], v[176:179], v[106:109]
	v_mfma_f32_16x16x32_bf16 v[94:97], v[130:133], v[184:187], v[94:97]
	v_mfma_f32_16x16x32_bf16 v[90:93], v[138:141], v[184:187], v[90:93]
	v_mfma_f32_16x16x32_bf16 v[78:81], v[130:133], v[192:195], v[78:81]
	v_mfma_f32_16x16x32_bf16 v[74:77], v[138:141], v[192:195], v[74:77]
	v_mfma_f32_16x16x32_bf16 v[126:129], v[134:137], v[166:169], v[126:129]
	v_mfma_f32_16x16x32_bf16 v[122:125], v[142:145], v[166:169], v[122:125]
	v_mfma_f32_16x16x32_bf16 v[110:113], v[134:137], v[180:183], v[110:113]
	v_mfma_f32_16x16x32_bf16 v[106:109], v[142:145], v[180:183], v[106:109]
	v_mfma_f32_16x16x32_bf16 v[94:97], v[134:137], v[188:191], v[94:97]
	v_mfma_f32_16x16x32_bf16 v[90:93], v[142:145], v[188:191], v[90:93]
	v_mfma_f32_16x16x32_bf16 v[78:81], v[134:137], v[196:199], v[78:81]
	v_mfma_f32_16x16x32_bf16 v[74:77], v[142:145], v[196:199], v[74:77]
	s_setprio 0
	s_barrier
	s_add_i32 s38, 0, 0x1c000
	s_add_i32 s39, s56, s5
	v_add_u32_e32 v175, s38, v171
	v_lshl_add_u64 v[218:219], v[218:219], 0, s[18:19]
	s_mov_b32 m0, s39
	ds_read_b128 v[200:203], v175
	ds_read_b128 v[204:207], v175 offset:1024
	ds_read_b128 v[208:211], v175 offset:2048
	ds_read_b128 v[214:217], v175 offset:3072
	global_load_lds_dwordx4 v[218:219], off
	v_lshl_add_u64 v[218:219], v[220:221], 0, s[18:19]
	s_add_i32 m0, s39, 0x2000
	s_nop 0
	global_load_lds_dwordx4 v[218:219], off
	s_barrier
	s_setprio 1
	s_waitcnt lgkmcnt(0)
	v_mfma_f32_16x16x32_bf16 v[118:121], v[200:203], v[162:165], v[118:121]
	v_mfma_f32_16x16x32_bf16 v[114:117], v[208:211], v[162:165], v[114:117]
	ds_read_b128 v[162:165], v173 offset:49152
	v_mfma_f32_16x16x32_bf16 v[102:105], v[200:203], v[176:179], v[102:105]
	v_mfma_f32_16x16x32_bf16 v[98:101], v[208:211], v[176:179], v[98:101]
	ds_read_b128 v[176:179], v173 offset:51200
	v_mfma_f32_16x16x32_bf16 v[86:89], v[200:203], v[184:187], v[86:89]
	v_mfma_f32_16x16x32_bf16 v[82:85], v[208:211], v[184:187], v[82:85]
	ds_read_b128 v[184:187], v173 offset:53248
	v_mfma_f32_16x16x32_bf16 v[70:73], v[200:203], v[192:195], v[70:73]
	v_mfma_f32_16x16x32_bf16 v[66:69], v[208:211], v[192:195], v[66:69]
	ds_read_b128 v[192:195], v173 offset:55296
	v_mfma_f32_16x16x32_bf16 v[118:121], v[204:207], v[166:169], v[118:121]
	v_mfma_f32_16x16x32_bf16 v[114:117], v[214:217], v[166:169], v[114:117]
	ds_read_b128 v[166:169], v173 offset:50176
	v_mfma_f32_16x16x32_bf16 v[102:105], v[204:207], v[180:183], v[102:105]
	v_mfma_f32_16x16x32_bf16 v[98:101], v[214:217], v[180:183], v[98:101]
	ds_read_b128 v[180:183], v173 offset:52224
	v_mfma_f32_16x16x32_bf16 v[86:89], v[204:207], v[188:191], v[86:89]
	v_mfma_f32_16x16x32_bf16 v[82:85], v[214:217], v[188:191], v[82:85]
	ds_read_b128 v[188:191], v173 offset:54272
	v_mfma_f32_16x16x32_bf16 v[70:73], v[204:207], v[196:199], v[70:73]
	v_mfma_f32_16x16x32_bf16 v[66:69], v[214:217], v[196:199], v[66:69]
	ds_read_b128 v[196:199], v173 offset:56320
	s_setprio 0
	s_mov_b32 m0, s44
	v_lshl_add_u64 v[218:219], v[222:223], 0, s[18:19]
	s_barrier
	global_load_lds_dwordx4 v[218:219], off
	v_lshl_add_u64 v[218:219], v[224:225], 0, s[18:19]
	s_mov_b32 m0, s45
	s_nop 0
	global_load_lds_dwordx4 v[218:219], off
	s_barrier
	s_setprio 1
	s_waitcnt lgkmcnt(0)
	v_mfma_f32_16x16x32_bf16 v[62:65], v[130:133], v[162:165], v[62:65]
	v_mfma_f32_16x16x32_bf16 v[58:61], v[138:141], v[162:165], v[58:61]
	v_mfma_f32_16x16x32_bf16 v[46:49], v[130:133], v[176:179], v[46:49]
	v_mfma_f32_16x16x32_bf16 v[42:45], v[138:141], v[176:179], v[42:45]
	v_mfma_f32_16x16x32_bf16 v[30:33], v[130:133], v[184:187], v[30:33]
	v_mfma_f32_16x16x32_bf16 v[26:29], v[138:141], v[184:187], v[26:29]
	v_mfma_f32_16x16x32_bf16 v[14:17], v[130:133], v[192:195], v[14:17]
	v_mfma_f32_16x16x32_bf16 v[10:13], v[138:141], v[192:195], v[10:13]
	v_mfma_f32_16x16x32_bf16 v[62:65], v[134:137], v[166:169], v[62:65]
	v_mfma_f32_16x16x32_bf16 v[58:61], v[142:145], v[166:169], v[58:61]
	v_mfma_f32_16x16x32_bf16 v[46:49], v[134:137], v[180:183], v[46:49]
	v_mfma_f32_16x16x32_bf16 v[42:45], v[142:145], v[180:183], v[42:45]
	v_mfma_f32_16x16x32_bf16 v[30:33], v[134:137], v[188:191], v[30:33]
	v_mfma_f32_16x16x32_bf16 v[26:29], v[142:145], v[188:191], v[26:29]
	v_mfma_f32_16x16x32_bf16 v[14:17], v[134:137], v[196:199], v[14:17]
	v_mfma_f32_16x16x32_bf16 v[10:13], v[142:145], v[196:199], v[10:13]
	s_setprio 0
	s_barrier
	s_add_u32 s36, s36, 0x80080
	s_addc_u32 s37, s37, 0
	s_add_i32 s38, s38, s5
	v_lshl_add_u64 v[130:131], s[36:37], 0, v[148:149]
	s_mov_b32 m0, s38
	s_nop 0
	global_load_lds_dwordx4 v[130:131], off
	v_lshl_add_u64 v[130:131], s[36:37], 0, v[152:153]
	s_add_i32 m0, s38, 0x2000
	s_nop 0
	global_load_lds_dwordx4 v[130:131], off
	s_waitcnt vmcnt(6)
	s_barrier
	s_setprio 1
	v_mfma_f32_16x16x32_bf16 v[54:57], v[200:203], v[162:165], v[54:57]
	ds_read_b128 v[130:133], v172
	ds_read_b128 v[134:137], v172 offset:1024
	ds_read_b128 v[138:141], v172 offset:2048
	ds_read_b128 v[142:145], v172 offset:3072
	v_mfma_f32_16x16x32_bf16 v[50:53], v[208:211], v[162:165], v[50:53]
	ds_read_b128 v[162:165], v173
	v_mfma_f32_16x16x32_bf16 v[38:41], v[200:203], v[176:179], v[38:41]
	v_mfma_f32_16x16x32_bf16 v[34:37], v[208:211], v[176:179], v[34:37]
	ds_read_b128 v[176:179], v173 offset:2048
	v_mfma_f32_16x16x32_bf16 v[22:25], v[200:203], v[184:187], v[22:25]
	v_mfma_f32_16x16x32_bf16 v[18:21], v[208:211], v[184:187], v[18:21]
	ds_read_b128 v[184:187], v173 offset:4096
	v_mfma_f32_16x16x32_bf16 v[6:9], v[200:203], v[192:195], v[6:9]
	v_mfma_f32_16x16x32_bf16 v[2:5], v[208:211], v[192:195], v[2:5]
	ds_read_b128 v[192:195], v173 offset:6144
	v_mfma_f32_16x16x32_bf16 v[54:57], v[204:207], v[166:169], v[54:57]
	v_mfma_f32_16x16x32_bf16 v[50:53], v[214:217], v[166:169], v[50:53]
	ds_read_b128 v[166:169], v173 offset:1024
	v_mfma_f32_16x16x32_bf16 v[38:41], v[204:207], v[180:183], v[38:41]
	v_mfma_f32_16x16x32_bf16 v[34:37], v[214:217], v[180:183], v[34:37]
	ds_read_b128 v[180:183], v173 offset:3072
	v_mfma_f32_16x16x32_bf16 v[22:25], v[204:207], v[188:191], v[22:25]
	v_mfma_f32_16x16x32_bf16 v[18:21], v[214:217], v[188:191], v[18:21]
	ds_read_b128 v[188:191], v173 offset:5120
	v_mfma_f32_16x16x32_bf16 v[6:9], v[204:207], v[196:199], v[6:9]
	v_mfma_f32_16x16x32_bf16 v[2:5], v[214:217], v[196:199], v[2:5]
	ds_read_b128 v[196:199], v173 offset:7168
	s_setprio 0
	s_add_u32 s8, s8, 0x100
	s_addc_u32 s9, s9, 0
	s_add_u32 s53, s53, 0x100
	s_addc_u32 s54, s54, 0
	s_cmp_ge_i32 s55, s1
	s_mov_b32 s36, s55
	s_barrier
	s_cbranch_scc0 .LBB0_964
	s_branch .Lmy_pl1_exit
.LBB0_964:
	s_add_i32 s55, s36, 2
	s_add_u32 s37, s8, 0xfff80080
	s_addc_u32 s38, s9, -1
	s_cmp_eq_u32 s46, s36
	s_cselect_b32 s36, s52, s53
	s_cselect_b32 s39, s25, s38
	s_cselect_b32 s38, s27, s37
	s_cselect_b32 s37, s51, s54
	v_lshl_add_u64 v[200:201], s[8:9], 0, v[154:155]
	s_add_i32 m0, s23, 0xc000
	global_load_lds_dwordx4 v[200:201], off
	v_lshl_add_u64 v[200:201], s[8:9], 0, v[156:157]
	s_add_i32 m0, s23, 0xe000
	s_nop 0
	global_load_lds_dwordx4 v[200:201], off
	s_waitcnt lgkmcnt(8)
	s_barrier
	s_setprio 1
	s_waitcnt lgkmcnt(0)
	v_mfma_f32_16x16x32_bf16 v[126:129], v[130:133], v[162:165], v[126:129]
	ds_read_b128 v[200:203], v174
	ds_read_b128 v[204:207], v174 offset:1024
	ds_read_b128 v[208:211], v174 offset:2048
	ds_read_b128 v[214:217], v174 offset:3072
	v_mfma_f32_16x16x32_bf16 v[122:125], v[138:141], v[162:165], v[122:125]
	v_mfma_f32_16x16x32_bf16 v[110:113], v[130:133], v[176:179], v[110:113]
	v_mfma_f32_16x16x32_bf16 v[106:109], v[138:141], v[176:179], v[106:109]
	v_mfma_f32_16x16x32_bf16 v[94:97], v[130:133], v[184:187], v[94:97]
	v_mfma_f32_16x16x32_bf16 v[90:93], v[138:141], v[184:187], v[90:93]
	v_mfma_f32_16x16x32_bf16 v[78:81], v[130:133], v[192:195], v[78:81]
	v_mfma_f32_16x16x32_bf16 v[74:77], v[138:141], v[192:195], v[74:77]
	v_mfma_f32_16x16x32_bf16 v[126:129], v[134:137], v[166:169], v[126:129]
	v_mfma_f32_16x16x32_bf16 v[122:125], v[142:145], v[166:169], v[122:125]
	v_mfma_f32_16x16x32_bf16 v[110:113], v[134:137], v[180:183], v[110:113]
	v_mfma_f32_16x16x32_bf16 v[106:109], v[142:145], v[180:183], v[106:109]
	v_mfma_f32_16x16x32_bf16 v[94:97], v[134:137], v[188:191], v[94:97]
	v_mfma_f32_16x16x32_bf16 v[90:93], v[142:145], v[188:191], v[90:93]
	v_mfma_f32_16x16x32_bf16 v[78:81], v[134:137], v[196:199], v[78:81]
	v_mfma_f32_16x16x32_bf16 v[74:77], v[142:145], v[196:199], v[74:77]
	s_setprio 0
	s_barrier
	s_add_i32 s56, s48, s5
	v_lshl_add_u64 v[218:219], s[36:37], 0, v[148:149]
	s_mov_b32 m0, s56
	global_load_lds_dwordx4 v[218:219], off
	v_lshl_add_u64 v[220:221], s[36:37], 0, v[152:153]
	s_add_i32 m0, s56, 0x2000
	s_nop 0
	global_load_lds_dwordx4 v[220:221], off
	s_barrier
	s_setprio 1
	s_waitcnt lgkmcnt(0)
	v_mfma_f32_16x16x32_bf16 v[118:121], v[200:203], v[162:165], v[118:121]
	v_mfma_f32_16x16x32_bf16 v[114:117], v[208:211], v[162:165], v[114:117]
	ds_read_b128 v[162:165], v173 offset:16384
	v_mfma_f32_16x16x32_bf16 v[102:105], v[200:203], v[176:179], v[102:105]
	v_mfma_f32_16x16x32_bf16 v[98:101], v[208:211], v[176:179], v[98:101]
	ds_read_b128 v[176:179], v173 offset:18432
	v_mfma_f32_16x16x32_bf16 v[86:89], v[200:203], v[184:187], v[86:89]
	v_mfma_f32_16x16x32_bf16 v[82:85], v[208:211], v[184:187], v[82:85]
	ds_read_b128 v[184:187], v173 offset:20480
	v_mfma_f32_16x16x32_bf16 v[70:73], v[200:203], v[192:195], v[70:73]
	v_mfma_f32_16x16x32_bf16 v[66:69], v[208:211], v[192:195], v[66:69]
	ds_read_b128 v[192:195], v173 offset:22528
	v_mfma_f32_16x16x32_bf16 v[118:121], v[204:207], v[166:169], v[118:121]
	v_mfma_f32_16x16x32_bf16 v[114:117], v[214:217], v[166:169], v[114:117]
	ds_read_b128 v[166:169], v173 offset:17408
	v_mfma_f32_16x16x32_bf16 v[102:105], v[204:207], v[180:183], v[102:105]
	v_mfma_f32_16x16x32_bf16 v[98:101], v[214:217], v[180:183], v[98:101]
	ds_read_b128 v[180:183], v173 offset:19456
	v_mfma_f32_16x16x32_bf16 v[86:89], v[204:207], v[188:191], v[86:89]
	v_mfma_f32_16x16x32_bf16 v[82:85], v[214:217], v[188:191], v[82:85]
	ds_read_b128 v[188:191], v173 offset:21504
	v_mfma_f32_16x16x32_bf16 v[70:73], v[204:207], v[196:199], v[70:73]
	v_mfma_f32_16x16x32_bf16 v[66:69], v[214:217], v[196:199], v[66:69]
	ds_read_b128 v[196:199], v173 offset:23552
	s_setprio 0
	s_mov_b32 m0, s23
	v_lshl_add_u64 v[222:223], s[38:39], 0, v[146:147]
	s_barrier
	global_load_lds_dwordx4 v[222:223], off
	v_lshl_add_u64 v[224:225], s[38:39], 0, v[150:151]
	s_mov_b32 m0, s33
	s_nop 0
	global_load_lds_dwordx4 v[224:225], off
	s_barrier
	s_setprio 1
	s_waitcnt lgkmcnt(0)
	v_mfma_f32_16x16x32_bf16 v[62:65], v[130:133], v[162:165], v[62:65]
	v_mfma_f32_16x16x32_bf16 v[58:61], v[138:141], v[162:165], v[58:61]
	v_mfma_f32_16x16x32_bf16 v[46:49], v[130:133], v[176:179], v[46:49]
	v_mfma_f32_16x16x32_bf16 v[42:45], v[138:141], v[176:179], v[42:45]
	v_mfma_f32_16x16x32_bf16 v[30:33], v[130:133], v[184:187], v[30:33]
	v_mfma_f32_16x16x32_bf16 v[26:29], v[138:141], v[184:187], v[26:29]
	v_mfma_f32_16x16x32_bf16 v[14:17], v[130:133], v[192:195], v[14:17]
	v_mfma_f32_16x16x32_bf16 v[10:13], v[138:141], v[192:195], v[10:13]
	v_mfma_f32_16x16x32_bf16 v[62:65], v[134:137], v[166:169], v[62:65]
	v_mfma_f32_16x16x32_bf16 v[58:61], v[142:145], v[166:169], v[58:61]
	v_mfma_f32_16x16x32_bf16 v[46:49], v[134:137], v[180:183], v[46:49]
	v_mfma_f32_16x16x32_bf16 v[42:45], v[142:145], v[180:183], v[42:45]
	v_mfma_f32_16x16x32_bf16 v[30:33], v[134:137], v[188:191], v[30:33]
	v_mfma_f32_16x16x32_bf16 v[26:29], v[142:145], v[188:191], v[26:29]
	v_mfma_f32_16x16x32_bf16 v[14:17], v[134:137], v[196:199], v[14:17]
	v_mfma_f32_16x16x32_bf16 v[10:13], v[142:145], v[196:199], v[10:13]
	s_setprio 0
	s_barrier
	s_add_u32 s56, s36, 0x80000
	s_addc_u32 s57, s37, 0
	s_add_i32 s58, s49, s5
	v_lshl_add_u64 v[130:131], s[56:57], 0, v[148:149]
	s_mov_b32 m0, s58
	s_nop 0
	global_load_lds_dwordx4 v[130:131], off
	v_lshl_add_u64 v[130:131], s[56:57], 0, v[152:153]
	s_add_i32 m0, s58, 0x2000
	s_nop 0
	global_load_lds_dwordx4 v[130:131], off
	s_waitcnt vmcnt(6)
	s_barrier
	s_setprio 1
	v_mfma_f32_16x16x32_bf16 v[54:57], v[200:203], v[162:165], v[54:57]
	v_mfma_f32_16x16x32_bf16 v[50:53], v[208:211], v[162:165], v[50:53]
	ds_read_b128 v[162:165], v173 offset:32768
	v_mfma_f32_16x16x32_bf16 v[38:41], v[200:203], v[176:179], v[38:41]
	v_mfma_f32_16x16x32_bf16 v[34:37], v[208:211], v[176:179], v[34:37]
	ds_read_b128 v[176:179], v173 offset:34816
	v_mfma_f32_16x16x32_bf16 v[22:25], v[200:203], v[184:187], v[22:25]
	v_mfma_f32_16x16x32_bf16 v[18:21], v[208:211], v[184:187], v[18:21]
	ds_read_b128 v[184:187], v173 offset:36864
	v_mfma_f32_16x16x32_bf16 v[6:9], v[200:203], v[192:195], v[6:9]
	v_mfma_f32_16x16x32_bf16 v[2:5], v[208:211], v[192:195], v[2:5]
	ds_read_b128 v[192:195], v173 offset:38912
	v_mfma_f32_16x16x32_bf16 v[54:57], v[204:207], v[166:169], v[54:57]
	v_mfma_f32_16x16x32_bf16 v[50:53], v[214:217], v[166:169], v[50:53]
	ds_read_b128 v[166:169], v173 offset:33792
	v_mfma_f32_16x16x32_bf16 v[38:41], v[204:207], v[180:183], v[38:41]
	v_mfma_f32_16x16x32_bf16 v[34:37], v[214:217], v[180:183], v[34:37]
	ds_read_b128 v[180:183], v173 offset:35840
	v_mfma_f32_16x16x32_bf16 v[22:25], v[204:207], v[188:191], v[22:25]
	v_mfma_f32_16x16x32_bf16 v[18:21], v[214:217], v[188:191], v[18:21]
	ds_read_b128 v[188:191], v173 offset:37888
	v_mfma_f32_16x16x32_bf16 v[6:9], v[204:207], v[196:199], v[6:9]
	v_mfma_f32_16x16x32_bf16 v[2:5], v[214:217], v[196:199], v[2:5]
	ds_read_b128 v[196:199], v173 offset:39936
	s_setprio 0
	s_add_i32 s56, 0, 0x18000
	v_add_u32_e32 v142, s56, v171
	s_barrier
	ds_read_b128 v[130:133], v142
	ds_read_b128 v[134:137], v142 offset:1024
	ds_read_b128 v[138:141], v142 offset:2048
	ds_read_b128 v[142:145], v142 offset:3072
	s_add_u32 s38, s38, 0x80000
	s_addc_u32 s39, s39, 0
	s_mov_b32 m0, s35
	v_lshl_add_u64 v[200:201], s[38:39], 0, v[146:147]
	global_load_lds_dwordx4 v[200:201], off
	v_lshl_add_u64 v[200:201], s[38:39], 0, v[150:151]
	s_mov_b32 m0, s40
	s_nop 0
	global_load_lds_dwordx4 v[200:201], off
	s_waitcnt lgkmcnt(8)
	s_barrier
	s_setprio 1
	s_waitcnt lgkmcnt(0)
	v_mfma_f32_16x16x32_bf16 v[126:129], v[130:133], v[162:165], v[126:129]
	v_mfma_f32_16x16x32_bf16 v[122:125], v[138:141], v[162:165], v[122:125]
	v_mfma_f32_16x16x32_bf16 v[110:113], v[130:133], v[176:179], v[110:113]
	v_mfma_f32_16x16x32_bf16 v[106:109], v[138:141], v[176:179], v[106:109]
	v_mfma_f32_16x16x32_bf16 v[94:97], v[130:133], v[184:187], v[94:97]
	v_mfma_f32_16x16x32_bf16 v[90:93], v[138:141], v[184:187], v[90:93]
	v_mfma_f32_16x16x32_bf16 v[78:81], v[130:133], v[192:195], v[78:81]
	v_mfma_f32_16x16x32_bf16 v[74:77], v[138:141], v[192:195], v[74:77]
	v_mfma_f32_16x16x32_bf16 v[126:129], v[134:137], v[166:169], v[126:129]
	v_mfma_f32_16x16x32_bf16 v[122:125], v[142:145], v[166:169], v[122:125]
	v_mfma_f32_16x16x32_bf16 v[110:113], v[134:137], v[180:183], v[110:113]
	v_mfma_f32_16x16x32_bf16 v[106:109], v[142:145], v[180:183], v[106:109]
	v_mfma_f32_16x16x32_bf16 v[94:97], v[134:137], v[188:191], v[94:97]
	v_mfma_f32_16x16x32_bf16 v[90:93], v[142:145], v[188:191], v[90:93]
	v_mfma_f32_16x16x32_bf16 v[78:81], v[134:137], v[196:199], v[78:81]
	v_mfma_f32_16x16x32_bf16 v[74:77], v[142:145], v[196:199], v[74:77]
	s_setprio 0
	s_barrier
	s_add_i32 s38, 0, 0x1c000
	s_add_i32 s39, s56, s5
	v_add_u32_e32 v175, s38, v171
	v_lshl_add_u64 v[218:219], v[218:219], 0, s[18:19]
	s_mov_b32 m0, s39
	ds_read_b128 v[200:203], v175
	ds_read_b128 v[204:207], v175 offset:1024
	ds_read_b128 v[208:211], v175 offset:2048
	ds_read_b128 v[214:217], v175 offset:3072
	global_load_lds_dwordx4 v[218:219], off
	v_lshl_add_u64 v[218:219], v[220:221], 0, s[18:19]
	s_add_i32 m0, s39, 0x2000
	s_nop 0
	global_load_lds_dwordx4 v[218:219], off
	s_barrier
	s_setprio 1
	s_waitcnt lgkmcnt(0)
	v_mfma_f32_16x16x32_bf16 v[118:121], v[200:203], v[162:165], v[118:121]
	v_mfma_f32_16x16x32_bf16 v[114:117], v[208:211], v[162:165], v[114:117]
	ds_read_b128 v[162:165], v173 offset:49152
	v_mfma_f32_16x16x32_bf16 v[102:105], v[200:203], v[176:179], v[102:105]
	v_mfma_f32_16x16x32_bf16 v[98:101], v[208:211], v[176:179], v[98:101]
	ds_read_b128 v[176:179], v173 offset:51200
	v_mfma_f32_16x16x32_bf16 v[86:89], v[200:203], v[184:187], v[86:89]
	v_mfma_f32_16x16x32_bf16 v[82:85], v[208:211], v[184:187], v[82:85]
	ds_read_b128 v[184:187], v173 offset:53248
	v_mfma_f32_16x16x32_bf16 v[70:73], v[200:203], v[192:195], v[70:73]
	v_mfma_f32_16x16x32_bf16 v[66:69], v[208:211], v[192:195], v[66:69]
	ds_read_b128 v[192:195], v173 offset:55296
	v_mfma_f32_16x16x32_bf16 v[118:121], v[204:207], v[166:169], v[118:121]
	v_mfma_f32_16x16x32_bf16 v[114:117], v[214:217], v[166:169], v[114:117]
	ds_read_b128 v[166:169], v173 offset:50176
	v_mfma_f32_16x16x32_bf16 v[102:105], v[204:207], v[180:183], v[102:105]
	v_mfma_f32_16x16x32_bf16 v[98:101], v[214:217], v[180:183], v[98:101]
	ds_read_b128 v[180:183], v173 offset:52224
	v_mfma_f32_16x16x32_bf16 v[86:89], v[204:207], v[188:191], v[86:89]
	v_mfma_f32_16x16x32_bf16 v[82:85], v[214:217], v[188:191], v[82:85]
	ds_read_b128 v[188:191], v173 offset:54272
	v_mfma_f32_16x16x32_bf16 v[70:73], v[204:207], v[196:199], v[70:73]
	v_mfma_f32_16x16x32_bf16 v[66:69], v[214:217], v[196:199], v[66:69]
	ds_read_b128 v[196:199], v173 offset:56320
	s_setprio 0
	s_mov_b32 m0, s44
	v_lshl_add_u64 v[218:219], v[222:223], 0, s[18:19]
	s_barrier
	global_load_lds_dwordx4 v[218:219], off
	v_lshl_add_u64 v[218:219], v[224:225], 0, s[18:19]
	s_mov_b32 m0, s45
	s_nop 0
	global_load_lds_dwordx4 v[218:219], off
	s_barrier
	s_setprio 1
	s_waitcnt lgkmcnt(0)
	v_mfma_f32_16x16x32_bf16 v[62:65], v[130:133], v[162:165], v[62:65]
	v_mfma_f32_16x16x32_bf16 v[58:61], v[138:141], v[162:165], v[58:61]
	v_mfma_f32_16x16x32_bf16 v[46:49], v[130:133], v[176:179], v[46:49]
	v_mfma_f32_16x16x32_bf16 v[42:45], v[138:141], v[176:179], v[42:45]
	v_mfma_f32_16x16x32_bf16 v[30:33], v[130:133], v[184:187], v[30:33]
	v_mfma_f32_16x16x32_bf16 v[26:29], v[138:141], v[184:187], v[26:29]
	v_mfma_f32_16x16x32_bf16 v[14:17], v[130:133], v[192:195], v[14:17]
	v_mfma_f32_16x16x32_bf16 v[10:13], v[138:141], v[192:195], v[10:13]
	v_mfma_f32_16x16x32_bf16 v[62:65], v[134:137], v[166:169], v[62:65]
	v_mfma_f32_16x16x32_bf16 v[58:61], v[142:145], v[166:169], v[58:61]
	v_mfma_f32_16x16x32_bf16 v[46:49], v[134:137], v[180:183], v[46:49]
	v_mfma_f32_16x16x32_bf16 v[42:45], v[142:145], v[180:183], v[42:45]
	v_mfma_f32_16x16x32_bf16 v[30:33], v[134:137], v[188:191], v[30:33]
	v_mfma_f32_16x16x32_bf16 v[26:29], v[142:145], v[188:191], v[26:29]
	v_mfma_f32_16x16x32_bf16 v[14:17], v[134:137], v[196:199], v[14:17]
	v_mfma_f32_16x16x32_bf16 v[10:13], v[142:145], v[196:199], v[10:13]
	s_setprio 0
	s_barrier
	s_add_u32 s36, s36, 0x80080
	s_addc_u32 s37, s37, 0
	s_add_i32 s38, s38, s5
	v_lshl_add_u64 v[130:131], s[36:37], 0, v[148:149]
	s_mov_b32 m0, s38
	s_nop 0
	global_load_lds_dwordx4 v[130:131], off
	v_lshl_add_u64 v[130:131], s[36:37], 0, v[152:153]
	s_add_i32 m0, s38, 0x2000
	s_nop 0
	global_load_lds_dwordx4 v[130:131], off
	s_waitcnt vmcnt(6)
	s_barrier
	s_setprio 1
	v_mfma_f32_16x16x32_bf16 v[54:57], v[200:203], v[162:165], v[54:57]
	ds_read_b128 v[130:133], v172
	ds_read_b128 v[134:137], v172 offset:1024
	ds_read_b128 v[138:141], v172 offset:2048
	ds_read_b128 v[142:145], v172 offset:3072
	v_mfma_f32_16x16x32_bf16 v[50:53], v[208:211], v[162:165], v[50:53]
	ds_read_b128 v[162:165], v173
	v_mfma_f32_16x16x32_bf16 v[38:41], v[200:203], v[176:179], v[38:41]
	v_mfma_f32_16x16x32_bf16 v[34:37], v[208:211], v[176:179], v[34:37]
	ds_read_b128 v[176:179], v173 offset:2048
	v_mfma_f32_16x16x32_bf16 v[22:25], v[200:203], v[184:187], v[22:25]
	v_mfma_f32_16x16x32_bf16 v[18:21], v[208:211], v[184:187], v[18:21]
	ds_read_b128 v[184:187], v173 offset:4096
	v_mfma_f32_16x16x32_bf16 v[6:9], v[200:203], v[192:195], v[6:9]
	v_mfma_f32_16x16x32_bf16 v[2:5], v[208:211], v[192:195], v[2:5]
	ds_read_b128 v[192:195], v173 offset:6144
	v_mfma_f32_16x16x32_bf16 v[54:57], v[204:207], v[166:169], v[54:57]
	v_mfma_f32_16x16x32_bf16 v[50:53], v[214:217], v[166:169], v[50:53]
	ds_read_b128 v[166:169], v173 offset:1024
	v_mfma_f32_16x16x32_bf16 v[38:41], v[204:207], v[180:183], v[38:41]
	v_mfma_f32_16x16x32_bf16 v[34:37], v[214:217], v[180:183], v[34:37]
	ds_read_b128 v[180:183], v173 offset:3072
	v_mfma_f32_16x16x32_bf16 v[22:25], v[204:207], v[188:191], v[22:25]
	v_mfma_f32_16x16x32_bf16 v[18:21], v[214:217], v[188:191], v[18:21]
	ds_read_b128 v[188:191], v173 offset:5120
	v_mfma_f32_16x16x32_bf16 v[6:9], v[204:207], v[196:199], v[6:9]
	v_mfma_f32_16x16x32_bf16 v[2:5], v[214:217], v[196:199], v[2:5]
	ds_read_b128 v[196:199], v173 offset:7168
	s_setprio 0
	s_add_u32 s8, s8, 0x100
	s_addc_u32 s9, s9, 0
	s_add_u32 s53, s53, 0x100
	s_addc_u32 s54, s54, 0
	s_cmp_ge_i32 s55, s1
	s_mov_b32 s36, s55
	s_barrier
	s_cbranch_scc0 .LBB0_964
.Lmy_pl1_exit:
	s_waitcnt lgkmcnt(0)
	s_branch .LBB0_955

.LBB0_1546:
	s_waitcnt lgkmcnt(0)
	v_mov_b32_e32 v7, v202
	v_mov_b32_e32 v3, v203
	v_lshlrev_b32_e32 v2, 7, v183
	v_lshlrev_b32_e32 v4, 3, v3
	s_lshl_b32 s26, s66, 11
	v_or_b32_e32 v2, s48, v2
	v_and_b32_e32 v4, -16, v4
	s_add_i32 s26, s52, s26
	v_add_u32_e32 v2, v2, v4
	v_lshl_add_u32 v4, v7, 2, s26
	v_add_u32_e32 v6, 0x400, v4
	v_mul_f32_e32 v4, 0xbfb8aa3b, v174
	v_exp_f32_e32 v8, v4
	v_mul_f32_e32 v4, 0xbfb8aa3b, v170
	v_exp_f32_e32 v9, v4
	v_mul_f32_e32 v10, 0xbfb8aa3b, v175
	v_add_f32_e32 v8, 1.0, v8
	v_rcp_f32_e32 v8, v8
	v_add_f32_e32 v9, 1.0, v9
	v_rcp_f32_e32 v9, v9
	v_exp_f32_e32 v10, v10
	v_mul_f32_e32 v8, v174, v8
	v_mul_f32_e32 v11, v158, v8
	v_mul_f32_e32 v8, v170, v9
	v_add_f32_e32 v9, 1.0, v10
	v_rcp_f32_e32 v9, v9
	v_mul_f32_e32 v10, 0xbfb8aa3b, v171
	v_exp_f32_e32 v10, v10
	v_mul_f32_e32 v13, v154, v8
	v_mul_f32_e32 v8, v175, v9
	v_mul_f32_e32 v9, 0xbfb8aa3b, v176
	v_mul_f32_e32 v14, v159, v8
	v_add_f32_e32 v8, 1.0, v10
	v_exp_f32_e32 v9, v9
	v_mul_f32_e32 v10, 0xbfb8aa3b, v172
	v_exp_f32_e32 v10, v10
	v_rcp_f32_e32 v8, v8
	v_add_f32_e32 v9, 1.0, v9
	ds_read2_b32 v[4:5], v6 offset1:16
	v_rcp_f32_e32 v9, v9
	v_add_f32_e32 v10, 1.0, v10
	v_rcp_f32_e32 v10, v10
	v_mul_f32_e32 v8, v171, v8
	v_mul_f32_e32 v15, v155, v8
	v_mul_f32_e32 v8, v176, v9
	v_mul_f32_e32 v16, v160, v8
	v_mul_f32_e32 v197, v172, v10
	s_waitcnt lgkmcnt(0)
	v_mov_b32_e32 v8, v4
	v_mov_b32_e32 v9, v156
	v_pk_mul_f32 v[8:9], v[8:9], v[196:197]
	v_lshlrev_b32_e32 v3, 4, v3
	v_mul_f32_e32 v4, v8, v11
	v_mul_f32_e32 v10, v8, v13
	v_mul_f32_e32 v11, v8, v14
	v_mul_f32_e32 v13, v8, v15
	v_mul_f32_e32 v14, 0xbfb8aa3b, v177
	v_mul_f32_e32 v15, v8, v16
	v_mul_f32_e32 v16, 0xbfb8aa3b, v173
	v_exp_f32_e32 v14, v14
	v_exp_f32_e32 v16, v16
	v_mul_f32_e32 v17, v8, v9
	v_and_b32_e32 v12, 16, v3
	v_add_f32_e32 v14, 1.0, v14
	v_add_f32_e32 v9, 1.0, v16
	v_rcp_f32_e32 v14, v14
	v_rcp_f32_e32 v9, v9
	v_ashrrev_i32_e32 v3, 31, v2
	s_cmp_eq_u32 s64, s33
	v_mul_f32_e32 v14, v177, v14
	v_mul_f32_e32 v9, v173, v9
	v_mul_f32_e32 v14, v161, v14
	v_mul_f32_e32 v9, v157, v9
	v_mul_f32_e32 v14, v8, v14
	v_mul_f32_e32 v16, v8, v9
	v_med3_f32 v8, v4, s58, v213
	v_med3_f32 v4, v11, s58, v213
	v_cvt_pk_fp8_f32 v8, v8, v4
	v_med3_f32 v9, v10, s58, v213
	v_med3_f32 v4, v13, s58, v213
	v_med3_f32 v11, v15, s58, v213
	v_med3_f32 v14, v14, s58, v213
	v_cvt_pk_fp8_f32 v9, v9, v4
	v_mul_f32_e32 v4, 0xbfb8aa3b, v166
	v_cvt_pk_fp8_f32 v8, v11, v14 op_sel:[0,0,1]
	v_exp_f32_e32 v4, v4
	v_mul_f32_e32 v11, 0xbfb8aa3b, v162
	v_exp_f32_e32 v11, v11
	v_med3_f32 v10, v17, s58, v213
	v_med3_f32 v13, v16, s58, v213
	v_add_f32_e32 v4, 1.0, v4
	v_cvt_pk_fp8_f32 v9, v10, v13 op_sel:[0,0,1]
	v_rcp_f32_e32 v4, v4
	v_add_f32_e32 v10, 1.0, v11
	v_mul_f32_e32 v11, 0xbfb8aa3b, v167
	v_rcp_f32_e32 v10, v10
	v_exp_f32_e32 v11, v11
	v_mul_f32_e32 v4, v166, v4
	v_mul_f32_e32 v13, v150, v4
	v_mul_f32_e32 v4, v162, v10
	v_add_f32_e32 v10, 1.0, v11
	v_rcp_f32_e32 v10, v10
	v_mul_f32_e32 v11, 0xbfb8aa3b, v163
	v_exp_f32_e32 v11, v11
	v_mul_f32_e32 v14, v146, v4
	v_mul_f32_e32 v4, v167, v10
	v_mul_f32_e32 v10, 0xbfb8aa3b, v168
	v_mul_f32_e32 v15, v151, v4
	v_add_f32_e32 v4, 1.0, v11
	v_exp_f32_e32 v10, v10
	v_mul_f32_e32 v11, 0xbfb8aa3b, v164
	v_exp_f32_e32 v11, v11
	v_rcp_f32_e32 v4, v4
	v_add_f32_e32 v10, 1.0, v10
	v_rcp_f32_e32 v10, v10
	v_add_f32_e32 v11, 1.0, v11
	v_rcp_f32_e32 v11, v11
	v_mul_f32_e32 v4, v163, v4
	v_mul_f32_e32 v16, v147, v4
	v_mul_f32_e32 v4, v168, v10
	v_mul_f32_e32 v17, v152, v4
	v_mul_f32_e32 v10, v164, v11
	v_mov_b32_e32 v4, v148
	v_mov_b32_e32 v11, v196
	v_pk_mul_f32 v[4:5], v[4:5], v[10:11]
	v_mov_b32_e32 v183, s14
	v_mul_f32_e32 v10, v13, v5
	v_mul_f32_e32 v11, v14, v5
	v_mul_f32_e32 v13, v15, v5
	v_mul_f32_e32 v14, v16, v5
	v_mul_f32_e32 v15, 0xbfb8aa3b, v169
	v_mul_f32_e32 v16, v17, v5
	v_mul_f32_e32 v17, 0xbfb8aa3b, v165
	v_exp_f32_e32 v15, v15
	v_exp_f32_e32 v17, v17
	v_med3_f32 v10, v10, s58, v213
	v_med3_f32 v13, v13, s58, v213
	v_add_f32_e32 v15, 1.0, v15
	v_add_f32_e32 v17, 1.0, v17
	v_rcp_f32_e32 v15, v15
	v_rcp_f32_e32 v17, v17
	v_med3_f32 v11, v11, s58, v213
	v_cvt_pk_fp8_f32 v10, v10, v13
	v_med3_f32 v13, v14, s58, v213
	v_mul_f32_e32 v15, v169, v15
	v_mul_f32_e32 v17, v165, v17
	v_cvt_pk_fp8_f32 v11, v11, v13
	v_mul_f32_e32 v15, v153, v15
	v_mul_f32_e32 v17, v149, v17
	v_mul_f32_e32 v4, v4, v5
	v_mul_f32_e32 v15, v15, v5
	v_mul_f32_e32 v5, v17, v5
	v_med3_f32 v4, v4, s58, v213
	v_med3_f32 v5, v5, s58, v213
	v_cvt_pk_fp8_f32 v11, v4, v5 op_sel:[0,0,1]
	v_lshlrev_b32_e32 v4, 8, v182
	v_med3_f32 v16, v16, s58, v213
	v_med3_f32 v15, v15, s58, v213
	v_add_u32_e32 v4, s47, v4
	v_cvt_pk_fp8_f32 v10, v16, v15 op_sel:[0,0,1]
	v_add3_u32 v4, v4, v7, v12
	v_ashrrev_i32_e32 v5, 31, v4
	v_lshlrev_b64 v[12:13], 9, v[4:5]
	v_lshl_add_u64 v[12:13], s[18:19], 0, v[12:13]
	v_permlane16_swap_b32_e32 v8, v10
	v_permlane16_swap_b32_e32 v9, v11
	v_lshl_add_u64 v[12:13], v[12:13], 0, v[2:3]
	global_store_dwordx4 v[12:13], v[8:11], off nt
	v_mul_f32_e32 v12, 0xbfb8aa3b, v132
	v_exp_f32_e32 v12, v12
	v_mul_f32_e32 v8, 0xbfb8aa3b, v143
	v_exp_f32_e32 v8, v8
	v_mul_f32_e32 v9, 0xbfb8aa3b, v131
	v_exp_f32_e32 v9, v9
	ds_read2_b32 v[10:11], v6 offset0:32 offset1:48
	v_add_f32_e32 v8, 1.0, v8
	v_rcp_f32_e32 v8, v8
	v_add_f32_e32 v12, 1.0, v12
	v_rcp_f32_e32 v12, v12
	s_waitcnt lgkmcnt(0)
	v_mov_b32_e32 v13, v10
	v_mul_f32_e32 v8, v143, v8
	v_mul_f32_e32 v14, v139, v8
	v_add_f32_e32 v8, 1.0, v9
	v_mul_f32_e32 v9, 0xbfb8aa3b, v144
	v_exp_f32_e32 v9, v9
	v_rcp_f32_e32 v8, v8
	v_mul_f32_e32 v5, 0xbfb8aa3b, v142
	v_exp_f32_e32 v5, v5
	v_add_f32_e32 v9, 1.0, v9
	v_rcp_f32_e32 v9, v9
	v_mul_f32_e32 v8, v131, v8
	v_mul_f32_e32 v15, v135, v8
	v_mul_f32_e32 v7, 0xbfb8aa3b, v130
	v_mul_f32_e32 v8, v144, v9
	v_mul_f32_e32 v16, v140, v8
	v_mul_f32_e32 v8, v132, v12
	v_mov_b32_e32 v12, v136
	v_mov_b32_e32 v9, v196
	v_pk_mul_f32 v[8:9], v[12:13], v[8:9]
	v_mul_f32_e32 v13, 0xbfb8aa3b, v145
	v_mul_f32_e32 v12, v15, v9
	v_mul_f32_e32 v15, 0xbfb8aa3b, v133
	v_exp_f32_e32 v15, v15
	v_add_f32_e32 v5, 1.0, v5
	v_exp_f32_e32 v13, v13
	v_exp_f32_e32 v7, v7
	v_rcp_f32_e32 v5, v5
	v_mul_f32_e32 v10, v14, v9
	v_mul_f32_e32 v14, v16, v9
	v_mul_f32_e32 v16, v8, v9
	v_add_f32_e32 v8, 1.0, v15
	v_rcp_f32_e32 v8, v8
	v_add_f32_e32 v13, 1.0, v13
	v_add_f32_e32 v7, 1.0, v7
	v_mul_f32_e32 v5, v142, v5
	v_rcp_f32_e32 v13, v13
	v_rcp_f32_e32 v7, v7
	v_mul_f32_e32 v5, v138, v5
	v_mul_f32_e32 v8, v133, v8
	v_mul_f32_e32 v5, v5, v9
	v_mul_f32_e32 v8, v137, v8
	v_mul_f32_e32 v15, v8, v9
	v_med3_f32 v8, v5, s58, v213
	v_med3_f32 v5, v10, s58, v213
	v_mul_f32_e32 v13, v145, v13
	v_cvt_pk_fp8_f32 v8, v8, v5
	v_mul_f32_e32 v7, v130, v7
	v_mul_f32_e32 v13, v141, v13
	v_mul_f32_e32 v7, v134, v7
	v_mul_f32_e32 v13, v13, v9
	v_mul_f32_e32 v7, v7, v9
	v_med3_f32 v10, v14, s58, v213
	v_med3_f32 v13, v13, s58, v213
	v_med3_f32 v9, v7, s58, v213
	v_med3_f32 v5, v12, s58, v213
	v_cvt_pk_fp8_f32 v8, v10, v13 op_sel:[0,0,1]
	v_mul_f32_e32 v10, 0xbfb8aa3b, v114
	v_cvt_pk_fp8_f32 v9, v9, v5
	v_exp_f32_e32 v10, v10
	v_med3_f32 v7, v16, s58, v213
	v_med3_f32 v12, v15, s58, v213
	v_cvt_pk_fp8_f32 v9, v7, v12 op_sel:[0,0,1]
	v_add_f32_e32 v7, 1.0, v10
	v_mul_f32_e32 v10, 0xbfb8aa3b, v119
	v_exp_f32_e32 v10, v10
	v_mul_f32_e32 v12, 0xbfb8aa3b, v115
	v_exp_f32_e32 v12, v12
	v_mul_f32_e32 v13, 0xbfb8aa3b, v116
	v_add_f32_e32 v10, 1.0, v10
	v_rcp_f32_e32 v10, v10
	v_exp_f32_e32 v13, v13
	v_mul_f32_e32 v5, 0xbfb8aa3b, v118
	v_exp_f32_e32 v5, v5
	v_mul_f32_e32 v10, v119, v10
	v_mul_f32_e32 v14, v127, v10
	v_add_f32_e32 v10, 1.0, v12
	v_mul_f32_e32 v12, 0xbfb8aa3b, v120
	v_exp_f32_e32 v12, v12
	v_rcp_f32_e32 v10, v10
	v_add_f32_e32 v13, 1.0, v13
	v_rcp_f32_e32 v13, v13
	v_add_f32_e32 v12, 1.0, v12
	v_rcp_f32_e32 v12, v12
	v_mul_f32_e32 v10, v115, v10
	v_mul_f32_e32 v15, v123, v10
	v_add_f32_e32 v5, 1.0, v5
	v_mul_f32_e32 v10, v120, v12
	v_mul_f32_e32 v16, v128, v10
	v_mul_f32_e32 v12, v116, v13
	v_mov_b32_e32 v10, v124
	v_mov_b32_e32 v13, v196
	v_pk_mul_f32 v[10:11], v[10:11], v[12:13]
	v_rcp_f32_e32 v5, v5
	v_mul_f32_e32 v13, v15, v11
	v_mul_f32_e32 v15, v16, v11
	v_mul_f32_e32 v16, 0xbfb8aa3b, v117
	v_mul_f32_e32 v12, v14, v11
	v_mul_f32_e32 v14, 0xbfb8aa3b, v121
	v_exp_f32_e32 v16, v16
	v_exp_f32_e32 v14, v14
	v_mul_f32_e32 v17, v10, v11
	v_rcp_f32_e32 v7, v7
	v_add_f32_e32 v10, 1.0, v16
	v_add_f32_e32 v14, 1.0, v14
	v_rcp_f32_e32 v10, v10
	v_rcp_f32_e32 v14, v14
	v_mul_f32_e32 v5, v118, v5
	v_mul_f32_e32 v5, v126, v5
	v_mul_f32_e32 v7, v114, v7
	v_mul_f32_e32 v10, v117, v10
	v_mul_f32_e32 v7, v122, v7
	v_mul_f32_e32 v5, v5, v11
	v_mul_f32_e32 v14, v121, v14
	v_mul_f32_e32 v10, v125, v10
	v_mul_f32_e32 v7, v7, v11
	v_mul_f32_e32 v14, v129, v14
	v_mul_f32_e32 v16, v10, v11
	v_med3_f32 v10, v5, s58, v213
	v_med3_f32 v5, v12, s58, v213
	v_mul_f32_e32 v14, v14, v11
	v_med3_f32 v11, v7, s58, v213
	v_cvt_pk_fp8_f32 v10, v10, v5
	v_med3_f32 v5, v13, s58, v213
	v_cvt_pk_fp8_f32 v11, v11, v5
	v_med3_f32 v12, v15, s58, v213
	v_med3_f32 v14, v14, s58, v213
	v_med3_f32 v5, v17, s58, v213
	v_med3_f32 v7, v16, s58, v213
	v_cvt_pk_fp8_f32 v10, v12, v14 op_sel:[0,0,1]
	v_cvt_pk_fp8_f32 v11, v5, v7 op_sel:[0,0,1]
	v_add_u32_e32 v12, 32, v4
	v_ashrrev_i32_e32 v13, 31, v12
	v_lshlrev_b64 v[12:13], 9, v[12:13]
	v_lshl_add_u64 v[12:13], s[18:19], 0, v[12:13]
	v_permlane16_swap_b32_e32 v8, v10
	v_permlane16_swap_b32_e32 v9, v11
	v_lshl_add_u64 v[12:13], v[12:13], 0, v[2:3]
	global_store_dwordx4 v[12:13], v[8:11], off nt
	v_mul_f32_e32 v12, 0xbfb8aa3b, v104
	v_exp_f32_e32 v12, v12
	v_mul_f32_e32 v8, 0xbfb8aa3b, v111
	v_exp_f32_e32 v8, v8
	v_mul_f32_e32 v9, 0xbfb8aa3b, v103
	v_exp_f32_e32 v9, v9
	ds_read2_b32 v[10:11], v6 offset0:128 offset1:144
	v_add_f32_e32 v8, 1.0, v8
	v_rcp_f32_e32 v8, v8
	v_add_f32_e32 v12, 1.0, v12
	v_rcp_f32_e32 v12, v12
	s_waitcnt lgkmcnt(0)
	v_mov_b32_e32 v13, v10
	v_mul_f32_e32 v8, v111, v8
	v_mul_f32_e32 v14, v107, v8
	v_add_f32_e32 v8, 1.0, v9
	v_mul_f32_e32 v9, 0xbfb8aa3b, v112
	v_exp_f32_e32 v9, v9
	v_rcp_f32_e32 v8, v8
	v_mul_f32_e32 v5, 0xbfb8aa3b, v110
	v_exp_f32_e32 v5, v5
	v_add_f32_e32 v9, 1.0, v9
	v_rcp_f32_e32 v9, v9
	v_mul_f32_e32 v8, v103, v8
	v_mul_f32_e32 v15, v99, v8
	v_mul_f32_e32 v7, 0xbfb8aa3b, v102
	v_mul_f32_e32 v8, v112, v9
	v_mul_f32_e32 v16, v108, v8
	v_mul_f32_e32 v8, v104, v12
	v_mov_b32_e32 v12, v100
	v_mov_b32_e32 v9, v196
	v_pk_mul_f32 v[8:9], v[12:13], v[8:9]
	v_mul_f32_e32 v13, 0xbfb8aa3b, v113
	v_mul_f32_e32 v12, v15, v9
	v_mul_f32_e32 v15, 0xbfb8aa3b, v105
	v_exp_f32_e32 v15, v15
	v_add_f32_e32 v5, 1.0, v5
	v_exp_f32_e32 v13, v13
	v_exp_f32_e32 v7, v7
	v_rcp_f32_e32 v5, v5
	v_mul_f32_e32 v10, v14, v9
	v_mul_f32_e32 v14, v16, v9
	v_mul_f32_e32 v16, v8, v9
	v_add_f32_e32 v8, 1.0, v15
	v_rcp_f32_e32 v8, v8
	v_add_f32_e32 v13, 1.0, v13
	v_add_f32_e32 v7, 1.0, v7
	v_mul_f32_e32 v5, v110, v5
	v_rcp_f32_e32 v13, v13
	v_rcp_f32_e32 v7, v7
	v_mul_f32_e32 v5, v106, v5
	v_mul_f32_e32 v8, v105, v8
	v_mul_f32_e32 v5, v5, v9
	v_mul_f32_e32 v8, v101, v8
	v_mul_f32_e32 v15, v8, v9
	v_med3_f32 v8, v5, s58, v213
	v_med3_f32 v5, v10, s58, v213
	v_mul_f32_e32 v13, v113, v13
	v_cvt_pk_fp8_f32 v8, v8, v5
	v_mul_f32_e32 v7, v102, v7
	v_mul_f32_e32 v13, v109, v13
	v_mul_f32_e32 v7, v98, v7
	v_mul_f32_e32 v13, v13, v9
	v_mul_f32_e32 v7, v7, v9
	v_med3_f32 v10, v14, s58, v213
	v_med3_f32 v13, v13, s58, v213
	v_med3_f32 v9, v7, s58, v213
	v_med3_f32 v5, v12, s58, v213
	v_cvt_pk_fp8_f32 v8, v10, v13 op_sel:[0,0,1]
	v_mul_f32_e32 v10, 0xbfb8aa3b, v86
	v_cvt_pk_fp8_f32 v9, v9, v5
	v_exp_f32_e32 v10, v10
	v_med3_f32 v7, v16, s58, v213
	v_med3_f32 v12, v15, s58, v213
	v_cvt_pk_fp8_f32 v9, v7, v12 op_sel:[0,0,1]
	v_add_f32_e32 v7, 1.0, v10
	v_mul_f32_e32 v10, 0xbfb8aa3b, v95
	v_exp_f32_e32 v10, v10
	v_mul_f32_e32 v12, 0xbfb8aa3b, v87
	v_exp_f32_e32 v12, v12
	v_mul_f32_e32 v13, 0xbfb8aa3b, v88
	v_add_f32_e32 v10, 1.0, v10
	v_rcp_f32_e32 v10, v10
	v_exp_f32_e32 v13, v13
	v_mul_f32_e32 v5, 0xbfb8aa3b, v94
	v_exp_f32_e32 v5, v5
	v_mul_f32_e32 v10, v95, v10
	v_mul_f32_e32 v14, v91, v10
	v_add_f32_e32 v10, 1.0, v12
	v_mul_f32_e32 v12, 0xbfb8aa3b, v96
	v_exp_f32_e32 v12, v12
	v_rcp_f32_e32 v10, v10
	v_add_f32_e32 v13, 1.0, v13
	v_rcp_f32_e32 v13, v13
	v_add_f32_e32 v12, 1.0, v12
	v_rcp_f32_e32 v12, v12
	v_mul_f32_e32 v10, v87, v10
	v_mul_f32_e32 v15, v83, v10
	v_add_f32_e32 v5, 1.0, v5
	v_mul_f32_e32 v10, v96, v12
	v_mul_f32_e32 v16, v92, v10
	v_mul_f32_e32 v12, v88, v13
	v_mov_b32_e32 v10, v84
	v_mov_b32_e32 v13, v196
	v_pk_mul_f32 v[10:11], v[10:11], v[12:13]
	v_rcp_f32_e32 v5, v5
	v_mul_f32_e32 v13, v15, v11
	v_mul_f32_e32 v15, v16, v11
	v_mul_f32_e32 v16, 0xbfb8aa3b, v89
	v_mul_f32_e32 v12, v14, v11
	v_mul_f32_e32 v14, 0xbfb8aa3b, v97
	v_exp_f32_e32 v16, v16
	v_exp_f32_e32 v14, v14
	v_mul_f32_e32 v17, v10, v11
	v_rcp_f32_e32 v7, v7
	v_add_f32_e32 v10, 1.0, v16
	v_add_f32_e32 v14, 1.0, v14
	v_rcp_f32_e32 v10, v10
	v_rcp_f32_e32 v14, v14
	v_mul_f32_e32 v5, v94, v5
	v_mul_f32_e32 v5, v90, v5
	v_mul_f32_e32 v7, v86, v7
	v_mul_f32_e32 v10, v89, v10
	v_mul_f32_e32 v7, v82, v7
	v_mul_f32_e32 v5, v5, v11
	v_mul_f32_e32 v14, v97, v14
	v_mul_f32_e32 v10, v85, v10
	v_mul_f32_e32 v7, v7, v11
	v_mul_f32_e32 v14, v93, v14
	v_mul_f32_e32 v16, v10, v11
	v_med3_f32 v10, v5, s58, v213
	v_med3_f32 v5, v12, s58, v213
	v_mul_f32_e32 v14, v14, v11
	v_med3_f32 v11, v7, s58, v213
	v_cvt_pk_fp8_f32 v10, v10, v5
	v_med3_f32 v5, v13, s58, v213
	v_cvt_pk_fp8_f32 v11, v11, v5
	v_med3_f32 v12, v15, s58, v213
	v_med3_f32 v14, v14, s58, v213
	v_med3_f32 v5, v17, s58, v213
	v_med3_f32 v7, v16, s58, v213
	v_cvt_pk_fp8_f32 v10, v12, v14 op_sel:[0,0,1]
	v_cvt_pk_fp8_f32 v11, v5, v7 op_sel:[0,0,1]
	v_add_u32_e32 v12, 0x80, v4
	v_mul_f32_e32 v7, 0xbfb8aa3b, v70
	v_ashrrev_i32_e32 v13, 31, v12
	v_exp_f32_e32 v7, v7
	v_lshlrev_b64 v[12:13], 9, v[12:13]
	v_lshl_add_u64 v[12:13], s[18:19], 0, v[12:13]
	v_permlane16_swap_b32_e32 v8, v10
	v_permlane16_swap_b32_e32 v9, v11
	v_lshl_add_u64 v[12:13], v[12:13], 0, v[2:3]
	global_store_dwordx4 v[12:13], v[8:11], off nt
	ds_read2_b32 v[8:9], v6 offset0:160 offset1:176
	v_add_f32_e32 v6, 1.0, v7
	v_mul_f32_e32 v7, 0xbfb8aa3b, v79
	v_exp_f32_e32 v7, v7
	v_rcp_f32_e32 v6, v6
	v_mul_f32_e32 v10, 0xbfb8aa3b, v71
	v_exp_f32_e32 v10, v10
	v_add_f32_e32 v7, 1.0, v7
	v_rcp_f32_e32 v7, v7
	v_mul_f32_e32 v6, v70, v6
	v_mul_f32_e32 v12, v66, v6
	s_waitcnt lgkmcnt(0)
	v_mov_b32_e32 v11, v8
	v_mul_f32_e32 v6, v79, v7
	v_mul_f32_e32 v7, 0xbfb8aa3b, v80
	v_mul_f32_e32 v13, v75, v6
	v_add_f32_e32 v6, 1.0, v10
	v_exp_f32_e32 v7, v7
	v_mul_f32_e32 v10, 0xbfb8aa3b, v72
	v_exp_f32_e32 v10, v10
	v_rcp_f32_e32 v6, v6
	v_add_f32_e32 v7, 1.0, v7
	v_rcp_f32_e32 v7, v7
	v_add_f32_e32 v10, 1.0, v10
	v_rcp_f32_e32 v10, v10
	v_mul_f32_e32 v6, v71, v6
	v_mul_f32_e32 v14, v67, v6
	v_mul_f32_e32 v6, v80, v7
	v_mul_f32_e32 v15, v76, v6
	v_mul_f32_e32 v6, v72, v10
	v_mov_b32_e32 v10, v68
	v_mov_b32_e32 v7, v196
	v_mul_f32_e32 v5, 0xbfb8aa3b, v78
	v_pk_mul_f32 v[6:7], v[10:11], v[6:7]
	v_exp_f32_e32 v5, v5
	v_mul_f32_e32 v11, v14, v7
	v_mul_f32_e32 v14, 0xbfb8aa3b, v73
	v_exp_f32_e32 v14, v14
	v_mul_f32_e32 v8, v12, v7
	v_mul_f32_e32 v12, 0xbfb8aa3b, v81
	v_add_f32_e32 v5, 1.0, v5
	v_exp_f32_e32 v12, v12
	v_rcp_f32_e32 v5, v5
	v_mul_f32_e32 v10, v13, v7
	v_mul_f32_e32 v13, v15, v7
	v_mul_f32_e32 v15, v6, v7
	v_add_f32_e32 v6, 1.0, v14
	v_rcp_f32_e32 v6, v6
	v_add_f32_e32 v12, 1.0, v12
	v_mul_f32_e32 v5, v78, v5
	v_rcp_f32_e32 v12, v12
	v_mul_f32_e32 v5, v74, v5
	v_mul_f32_e32 v6, v73, v6
	v_mul_f32_e32 v5, v5, v7
	v_mul_f32_e32 v6, v69, v6
	v_mul_f32_e32 v14, v6, v7
	v_med3_f32 v6, v5, s58, v213
	v_med3_f32 v5, v10, s58, v213
	v_mul_f32_e32 v12, v81, v12
	v_cvt_pk_fp8_f32 v6, v6, v5
	v_mul_f32_e32 v12, v77, v12
	v_mul_f32_e32 v12, v12, v7
	v_med3_f32 v10, v13, s58, v213
	v_med3_f32 v12, v12, s58, v213
	v_med3_f32 v7, v8, s58, v213
	v_med3_f32 v5, v11, s58, v213
	v_cvt_pk_fp8_f32 v6, v10, v12 op_sel:[0,0,1]
	v_mul_f32_e32 v10, 0xbfb8aa3b, v54
	v_cvt_pk_fp8_f32 v7, v7, v5
	v_exp_f32_e32 v10, v10
	v_med3_f32 v8, v15, s58, v213
	v_med3_f32 v11, v14, s58, v213
	v_cvt_pk_fp8_f32 v7, v8, v11 op_sel:[0,0,1]
	v_add_f32_e32 v8, 1.0, v10
	v_mul_f32_e32 v10, 0xbfb8aa3b, v63
	v_exp_f32_e32 v10, v10
	v_rcp_f32_e32 v8, v8
	v_mul_f32_e32 v11, 0xbfb8aa3b, v55
	v_exp_f32_e32 v11, v11
	v_add_f32_e32 v10, 1.0, v10
	v_rcp_f32_e32 v10, v10
	v_mul_f32_e32 v8, v54, v8
	v_mul_f32_e32 v12, v50, v8
	v_mul_f32_e32 v5, 0xbfb8aa3b, v62
	v_mul_f32_e32 v8, v63, v10
	v_mul_f32_e32 v10, 0xbfb8aa3b, v64
	v_mul_f32_e32 v13, v59, v8
	v_add_f32_e32 v8, 1.0, v11
	v_exp_f32_e32 v10, v10
	v_mul_f32_e32 v11, 0xbfb8aa3b, v56
	v_exp_f32_e32 v11, v11
	v_rcp_f32_e32 v8, v8
	v_add_f32_e32 v10, 1.0, v10
	v_rcp_f32_e32 v10, v10
	v_add_f32_e32 v11, 1.0, v11
	v_rcp_f32_e32 v11, v11
	v_mul_f32_e32 v8, v55, v8
	v_mul_f32_e32 v14, v51, v8
	v_mul_f32_e32 v8, v64, v10
	v_mul_f32_e32 v15, v60, v8
	v_mul_f32_e32 v10, v56, v11
	v_mov_b32_e32 v8, v52
	v_mov_b32_e32 v11, v196
	v_pk_mul_f32 v[8:9], v[8:9], v[10:11]
	v_exp_f32_e32 v5, v5
	v_mul_f32_e32 v10, v12, v9
	v_mul_f32_e32 v12, v14, v9
	v_mul_f32_e32 v14, v15, v9
	v_mul_f32_e32 v15, 0xbfb8aa3b, v57
	v_mul_f32_e32 v11, v13, v9
	v_mul_f32_e32 v13, 0xbfb8aa3b, v65
	v_exp_f32_e32 v15, v15
	v_exp_f32_e32 v13, v13
	v_add_f32_e32 v5, 1.0, v5
	v_rcp_f32_e32 v5, v5
	v_mul_f32_e32 v16, v8, v9
	v_add_f32_e32 v8, 1.0, v15
	v_add_f32_e32 v13, 1.0, v13
	v_rcp_f32_e32 v8, v8
	v_rcp_f32_e32 v13, v13
	v_mul_f32_e32 v5, v62, v5
	v_mul_f32_e32 v5, v58, v5
	v_mul_f32_e32 v8, v57, v8
	v_mul_f32_e32 v5, v5, v9
	v_mul_f32_e32 v13, v65, v13
	v_mul_f32_e32 v8, v53, v8
	v_mul_f32_e32 v13, v61, v13
	v_mul_f32_e32 v15, v8, v9
	v_med3_f32 v8, v5, s58, v213
	v_med3_f32 v5, v11, s58, v213
	v_mul_f32_e32 v13, v13, v9
	v_med3_f32 v9, v10, s58, v213
	v_cvt_pk_fp8_f32 v8, v8, v5
	v_med3_f32 v5, v12, s58, v213
	v_cvt_pk_fp8_f32 v9, v9, v5
	v_med3_f32 v11, v14, s58, v213
	v_med3_f32 v13, v13, s58, v213
	v_med3_f32 v5, v16, s58, v213
	v_med3_f32 v10, v15, s58, v213
	v_cvt_pk_fp8_f32 v8, v11, v13 op_sel:[0,0,1]
	v_cvt_pk_fp8_f32 v9, v5, v10 op_sel:[0,0,1]
	v_add_u32_e32 v4, 0xa0, v4
	v_ashrrev_i32_e32 v5, 31, v4
	v_lshlrev_b64 v[4:5], 9, v[4:5]
	v_lshl_add_u64 v[4:5], s[18:19], 0, v[4:5]
	v_permlane16_swap_b32_e32 v6, v8
	v_permlane16_swap_b32_e32 v7, v9
	v_lshl_add_u64 v[2:3], v[4:5], 0, v[2:3]
	v_mov_b32_e32 v182, v178
	s_mov_b32 s66, s65
	s_mov_b64 s[28:29], s[24:25]
	global_store_dwordx4 v[2:3], v[6:9], off nt
	s_cbranch_scc1 .LBB0_1555

.Lmy_pl2_1553:
	s_add_i32 s71, s71, 2
	s_add_u32 s30, s28, 0x100
	s_addc_u32 s31, s29, 0
	s_and_b64 s[36:37], s[34:35], exec
	s_cselect_b32 s36, 0, s30
	s_cselect_b32 s37, 0, s31
	s_add_u32 s36, s22, s36
	s_addc_u32 s37, s23, s37
	s_add_u32 s72, s69, s28
	s_addc_u32 s73, s70, s29
	s_and_b64 s[28:29], s[34:35], exec
	s_cselect_b32 s29, s67, s73
	s_cselect_b32 s28, s68, s72
	s_mov_b32 m0, s42
	v_add_u32_e32 v191, s57, v204
	v_lshl_add_u64 v[230:231], s[28:29], 0, v[188:189]
	v_add_u32_e32 v197, s57, v205
	ds_read_b128 v[214:217], v191
	ds_read_b128 v[222:225], v191 offset:2048
	ds_read_b128 v[218:221], v197
	ds_read_b128 v[226:229], v197 offset:2048
	global_load_lds_dwordx4 v[230:231], off
	v_lshl_add_u64 v[232:233], s[28:29], 0, v[186:187]
	s_mov_b32 m0, s43
	v_mfma_scale_f32_16x16x128_f8f6f4 v[174:177], v[2:9], v[26:33], 0, v211, v210 op_sel_hi:[0,0,0]
	global_load_lds_dwordx4 v[232:233], off
	s_barrier
	v_mov_b32_e32 v193, v185
	v_mov_b32_e32 v195, v185
	v_mfma_scale_f32_16x16x128_f8f6f4 v[170:173], v[10:17], v[26:33], 0, v211, v210 op_sel_hi:[0,0,0]
	v_mfma_scale_f32_16x16x128_f8f6f4 v[166:169], v[2:9], v[18:25], 0, v211, v210 op_sel_hi:[0,0,0]
	v_mfma_scale_f32_16x16x128_f8f6f4 v[162:165], v[10:17], v[18:25], 0, v211, v210 op_sel_hi:[0,0,0]
	v_mfma_scale_f32_16x16x128_f8f6f4 v[142:145], v[2:9], v[42:49], 0, v211, v210 op_sel_hi:[0,0,0]
	v_mfma_scale_f32_16x16x128_f8f6f4 v[130:133], v[10:17], v[42:49], 0, v211, v210 op_sel_hi:[0,0,0]
	v_mfma_scale_f32_16x16x128_f8f6f4 v[118:121], v[2:9], v[34:41], 0, v211, v210 op_sel_hi:[0,0,0]
	v_mfma_scale_f32_16x16x128_f8f6f4 v[114:117], v[10:17], v[34:41], 0, v211, v210 op_sel_hi:[0,0,0]
	s_setprio 1
	s_waitcnt lgkmcnt(0)
	v_mfma_scale_f32_16x16x128_f8f6f4 v[158:161], v[214:221], v[26:33], 0, v211, v210 op_sel_hi:[0,0,0]
	v_mfma_scale_f32_16x16x128_f8f6f4 v[154:157], v[222:229], v[26:33], 0, v211, v210 op_sel_hi:[0,0,0]
	ds_read_b128 v[26:29], v208 offset:18432
	ds_read_b128 v[30:33], v209 offset:18432
	v_mfma_scale_f32_16x16x128_f8f6f4 v[150:153], v[214:221], v[18:25], 0, v211, v210 op_sel_hi:[0,0,0]
	v_mfma_scale_f32_16x16x128_f8f6f4 v[146:149], v[222:229], v[18:25], 0, v211, v210 op_sel_hi:[0,0,0]
	ds_read_b128 v[18:21], v208 offset:16384
	ds_read_b128 v[22:25], v209 offset:16384
	v_mfma_scale_f32_16x16x128_f8f6f4 v[138:141], v[214:221], v[42:49], 0, v211, v210 op_sel_hi:[0,0,0]
	v_mfma_scale_f32_16x16x128_f8f6f4 v[134:137], v[222:229], v[42:49], 0, v211, v210 op_sel_hi:[0,0,0]
	ds_read_b128 v[42:45], v208 offset:22528
	ds_read_b128 v[46:49], v209 offset:22528
	v_mfma_scale_f32_16x16x128_f8f6f4 v[126:129], v[214:221], v[34:41], 0, v211, v210 op_sel_hi:[0,0,0]
	v_mfma_scale_f32_16x16x128_f8f6f4 v[122:125], v[222:229], v[34:41], 0, v211, v210 op_sel_hi:[0,0,0]
	ds_read_b128 v[34:37], v208 offset:20480
	ds_read_b128 v[38:41], v209 offset:20480
	s_setprio 0
	s_mov_b32 m0, s41
	s_barrier
	global_load_lds_dwordx4 v184, s[36:37]
	s_mov_b32 m0, s44
	v_mov_b32_e32 v191, v185
	global_load_lds_dwordx4 v190, s[36:37]
	s_barrier
	v_lshl_add_u64 v[234:235], s[36:37], 0, v[184:185]
	v_lshl_add_u64 v[236:237], s[36:37], 0, v[190:191]
	s_setprio 1
	s_waitcnt lgkmcnt(0)
	v_mfma_scale_f32_16x16x128_f8f6f4 v[110:113], v[2:9], v[18:25], 0, v211, v210 op_sel_hi:[0,0,0]
	v_mfma_scale_f32_16x16x128_f8f6f4 v[102:105], v[10:17], v[18:25], 0, v211, v210 op_sel_hi:[0,0,0]
	v_mfma_scale_f32_16x16x128_f8f6f4 v[94:97], v[2:9], v[26:33], 0, v211, v210 op_sel_hi:[0,0,0]
	v_mfma_scale_f32_16x16x128_f8f6f4 v[86:89], v[10:17], v[26:33], 0, v211, v210 op_sel_hi:[0,0,0]
	v_mfma_scale_f32_16x16x128_f8f6f4 v[78:81], v[2:9], v[34:41], 0, v211, v210 op_sel_hi:[0,0,0]
	v_mfma_scale_f32_16x16x128_f8f6f4 v[70:73], v[10:17], v[34:41], 0, v211, v210 op_sel_hi:[0,0,0]
	v_mfma_scale_f32_16x16x128_f8f6f4 v[62:65], v[2:9], v[42:49], 0, v211, v210 op_sel_hi:[0,0,0]
	v_mfma_scale_f32_16x16x128_f8f6f4 v[54:57], v[10:17], v[42:49], 0, v211, v210 op_sel_hi:[0,0,0]
	s_setprio 0
	s_barrier
	s_add_u32 s34, s28, 0x40000
	s_addc_u32 s35, s29, 0
	s_mov_b32 m0, s59
	v_lshl_add_u64 v[2:3], s[34:35], 0, v[188:189]
	global_load_lds_dwordx4 v[2:3], off
	v_lshl_add_u64 v[2:3], s[34:35], 0, v[186:187]
	s_mov_b32 m0, s60
	s_nop 0
	global_load_lds_dwordx4 v[2:3], off
	s_waitcnt vmcnt(6)
	s_barrier
	s_setprio 1
	v_mfma_scale_f32_16x16x128_f8f6f4 v[106:109], v[214:221], v[18:25], 0, v211, v210 op_sel_hi:[0,0,0]
	v_mfma_scale_f32_16x16x128_f8f6f4 v[98:101], v[222:229], v[18:25], 0, v211, v210 op_sel_hi:[0,0,0]
	ds_read_b128 v[18:21], v208 offset:32768
	ds_read_b128 v[22:25], v209 offset:32768
	v_mfma_scale_f32_16x16x128_f8f6f4 v[90:93], v[214:221], v[26:33], 0, v211, v210 op_sel_hi:[0,0,0]
	v_mfma_scale_f32_16x16x128_f8f6f4 v[82:85], v[222:229], v[26:33], 0, v211, v210 op_sel_hi:[0,0,0]
	ds_read_b128 v[26:29], v208 offset:34816
	ds_read_b128 v[30:33], v209 offset:34816
	v_mfma_scale_f32_16x16x128_f8f6f4 v[74:77], v[214:221], v[34:41], 0, v211, v210 op_sel_hi:[0,0,0]
	v_mfma_scale_f32_16x16x128_f8f6f4 v[66:69], v[222:229], v[34:41], 0, v211, v210 op_sel_hi:[0,0,0]
	ds_read_b128 v[34:37], v208 offset:36864
	ds_read_b128 v[38:41], v209 offset:36864
	v_mfma_scale_f32_16x16x128_f8f6f4 v[58:61], v[214:221], v[42:49], 0, v211, v210 op_sel_hi:[0,0,0]
	v_mfma_scale_f32_16x16x128_f8f6f4 v[50:53], v[222:229], v[42:49], 0, v211, v210 op_sel_hi:[0,0,0]
	ds_read_b128 v[42:45], v208 offset:38912
	ds_read_b128 v[46:49], v209 offset:38912
	s_setprio 0
	v_add_u32_e32 v6, s61, v204
	v_add_u32_e32 v14, s61, v205
	s_barrier
	ds_read_b128 v[2:5], v6
	ds_read_b128 v[10:13], v6 offset:2048
	ds_read_b128 v[6:9], v14
	ds_read_b128 v[14:17], v14 offset:2048
	s_mov_b32 m0, s45
	v_lshl_add_u64 v[214:215], s[36:37], 0, v[192:193]
	global_load_lds_dwordx4 v[214:215], off
	v_lshl_add_u64 v[214:215], s[36:37], 0, v[194:195]
	s_mov_b32 m0, s46
	s_nop 0
	global_load_lds_dwordx4 v[214:215], off
	s_waitcnt lgkmcnt(8)
	s_barrier
	s_setprio 1
	s_waitcnt lgkmcnt(0)
	v_mfma_scale_f32_16x16x128_f8f6f4 v[174:177], v[2:9], v[18:25], v[174:177], v211, v210 op_sel_hi:[0,0,0]
	v_mfma_scale_f32_16x16x128_f8f6f4 v[170:173], v[10:17], v[18:25], v[170:173], v211, v210 op_sel_hi:[0,0,0]
	v_mfma_scale_f32_16x16x128_f8f6f4 v[166:169], v[2:9], v[26:33], v[166:169], v211, v210 op_sel_hi:[0,0,0]
	v_mfma_scale_f32_16x16x128_f8f6f4 v[162:165], v[10:17], v[26:33], v[162:165], v211, v210 op_sel_hi:[0,0,0]
	v_mfma_scale_f32_16x16x128_f8f6f4 v[142:145], v[2:9], v[34:41], v[142:145], v211, v210 op_sel_hi:[0,0,0]
	v_mfma_scale_f32_16x16x128_f8f6f4 v[130:133], v[10:17], v[34:41], v[130:133], v211, v210 op_sel_hi:[0,0,0]
	v_mfma_scale_f32_16x16x128_f8f6f4 v[118:121], v[2:9], v[42:49], v[118:121], v211, v210 op_sel_hi:[0,0,0]
	v_mfma_scale_f32_16x16x128_f8f6f4 v[114:117], v[10:17], v[42:49], v[114:117], v211, v210 op_sel_hi:[0,0,0]
	s_setprio 0
	s_barrier
	s_mov_b32 m0, s63
	v_add_u32_e32 v191, s62, v204
	v_lshl_add_u64 v[230:231], v[230:231], 0, s[12:13]
	v_add_u32_e32 v193, s62, v205
	ds_read_b128 v[214:217], v191
	ds_read_b128 v[222:225], v191 offset:2048
	ds_read_b128 v[218:221], v193
	ds_read_b128 v[226:229], v193 offset:2048
	global_load_lds_dwordx4 v[230:231], off
	v_lshl_add_u64 v[230:231], v[232:233], 0, s[12:13]
	s_add_i32 m0, s63, 0x2000
	s_nop 0
	global_load_lds_dwordx4 v[230:231], off
	s_barrier
	s_setprio 1
	s_waitcnt lgkmcnt(0)
	v_mfma_scale_f32_16x16x128_f8f6f4 v[158:161], v[214:221], v[18:25], v[158:161], v211, v210 op_sel_hi:[0,0,0]
	v_mfma_scale_f32_16x16x128_f8f6f4 v[154:157], v[222:229], v[18:25], v[154:157], v211, v210 op_sel_hi:[0,0,0]
	ds_read_b128 v[18:21], v208 offset:49152
	ds_read_b128 v[22:25], v209 offset:49152
	v_mfma_scale_f32_16x16x128_f8f6f4 v[150:153], v[214:221], v[26:33], v[150:153], v211, v210 op_sel_hi:[0,0,0]
	v_mfma_scale_f32_16x16x128_f8f6f4 v[146:149], v[222:229], v[26:33], v[146:149], v211, v210 op_sel_hi:[0,0,0]
	ds_read_b128 v[26:29], v208 offset:51200
	ds_read_b128 v[30:33], v209 offset:51200
	v_mfma_scale_f32_16x16x128_f8f6f4 v[138:141], v[214:221], v[34:41], v[138:141], v211, v210 op_sel_hi:[0,0,0]
	v_mfma_scale_f32_16x16x128_f8f6f4 v[134:137], v[222:229], v[34:41], v[134:137], v211, v210 op_sel_hi:[0,0,0]
	ds_read_b128 v[34:37], v208 offset:53248
	ds_read_b128 v[38:41], v209 offset:53248
	v_mfma_scale_f32_16x16x128_f8f6f4 v[126:129], v[214:221], v[42:49], v[126:129], v211, v210 op_sel_hi:[0,0,0]
	v_mfma_scale_f32_16x16x128_f8f6f4 v[122:125], v[222:229], v[42:49], v[122:125], v211, v210 op_sel_hi:[0,0,0]
	ds_read_b128 v[42:45], v208 offset:55296
	ds_read_b128 v[46:49], v209 offset:55296
	s_setprio 0
	s_mov_b32 m0, s49
	v_lshl_add_u64 v[230:231], v[234:235], 0, s[12:13]
	s_barrier
	global_load_lds_dwordx4 v[230:231], off
	v_lshl_add_u64 v[230:231], v[236:237], 0, s[12:13]
	s_mov_b32 m0, s50
	s_nop 0
	global_load_lds_dwordx4 v[230:231], off
	s_barrier
	s_setprio 1
	s_waitcnt lgkmcnt(0)
	v_mfma_scale_f32_16x16x128_f8f6f4 v[110:113], v[2:9], v[18:25], v[110:113], v211, v210 op_sel_hi:[0,0,0]
	v_mfma_scale_f32_16x16x128_f8f6f4 v[102:105], v[10:17], v[18:25], v[102:105], v211, v210 op_sel_hi:[0,0,0]
	v_mfma_scale_f32_16x16x128_f8f6f4 v[94:97], v[2:9], v[26:33], v[94:97], v211, v210 op_sel_hi:[0,0,0]
	v_mfma_scale_f32_16x16x128_f8f6f4 v[86:89], v[10:17], v[26:33], v[86:89], v211, v210 op_sel_hi:[0,0,0]
	v_mfma_scale_f32_16x16x128_f8f6f4 v[78:81], v[2:9], v[34:41], v[78:81], v211, v210 op_sel_hi:[0,0,0]
	v_mfma_scale_f32_16x16x128_f8f6f4 v[70:73], v[10:17], v[34:41], v[70:73], v211, v210 op_sel_hi:[0,0,0]
	v_mfma_scale_f32_16x16x128_f8f6f4 v[62:65], v[2:9], v[42:49], v[62:65], v211, v210 op_sel_hi:[0,0,0]
	v_mfma_scale_f32_16x16x128_f8f6f4 v[54:57], v[10:17], v[42:49], v[54:57], v211, v210 op_sel_hi:[0,0,0]
	s_setprio 0
	s_barrier
	s_add_u32 s28, s28, 0x40080
	s_addc_u32 s29, s29, 0
	s_add_i32 s34, s62, s40
	v_lshl_add_u64 v[2:3], s[28:29], 0, v[188:189]
	s_mov_b32 m0, s34
	s_nop 0
	global_load_lds_dwordx4 v[2:3], off
	v_lshl_add_u64 v[2:3], s[28:29], 0, v[186:187]
	s_add_i32 m0, s34, 0x2000
	s_nop 0
	global_load_lds_dwordx4 v[2:3], off
	s_waitcnt vmcnt(6)
	s_barrier
	s_setprio 1
	v_mfma_scale_f32_16x16x128_f8f6f4 v[106:109], v[214:221], v[18:25], v[106:109], v211, v210 op_sel_hi:[0,0,0]
	ds_read_b128 v[2:5], v206
	ds_read_b128 v[10:13], v206 offset:2048
	ds_read_b128 v[6:9], v207
	ds_read_b128 v[14:17], v207 offset:2048
	v_mfma_scale_f32_16x16x128_f8f6f4 v[98:101], v[222:229], v[18:25], v[98:101], v211, v210 op_sel_hi:[0,0,0]
	ds_read_b128 v[18:21], v208 offset:2048
	ds_read_b128 v[22:25], v209 offset:2048
	v_mfma_scale_f32_16x16x128_f8f6f4 v[90:93], v[214:221], v[26:33], v[90:93], v211, v210 op_sel_hi:[0,0,0]
	v_mfma_scale_f32_16x16x128_f8f6f4 v[82:85], v[222:229], v[26:33], v[82:85], v211, v210 op_sel_hi:[0,0,0]
	ds_read_b128 v[26:29], v208
	ds_read_b128 v[30:33], v209
	v_mfma_scale_f32_16x16x128_f8f6f4 v[74:77], v[214:221], v[34:41], v[74:77], v211, v210 op_sel_hi:[0,0,0]
	v_mfma_scale_f32_16x16x128_f8f6f4 v[66:69], v[222:229], v[34:41], v[66:69], v211, v210 op_sel_hi:[0,0,0]
	ds_read_b128 v[34:37], v208 offset:6144
	ds_read_b128 v[38:41], v209 offset:6144
	v_mfma_scale_f32_16x16x128_f8f6f4 v[58:61], v[214:221], v[42:49], v[58:61], v211, v210 op_sel_hi:[0,0,0]
	v_mfma_scale_f32_16x16x128_f8f6f4 v[50:53], v[222:229], v[42:49], v[50:53], v211, v210 op_sel_hi:[0,0,0]
	ds_read_b128 v[42:45], v208 offset:4096
	ds_read_b128 v[46:49], v209 offset:4096
	s_setprio 0
	s_cmp_ge_i32 s71, s39
	s_barrier
	s_cbranch_scc1 .LBB0_1546
	s_mov_b64 s[28:29], s[30:31]
	s_branch .LBB0_1551
.LBB0_1551:
	s_cmp_eq_u32 s51, s71
	s_cselect_b64 s[34:35], -1, 0
	s_add_u32 s30, s53, s28
	s_addc_u32 s31, s54, s29
	s_mov_b32 m0, s55
	global_load_lds_dwordx4 v192, s[30:31]
	s_mov_b32 m0, s56
	s_nop 0
	global_load_lds_dwordx4 v194, s[30:31]
	s_waitcnt lgkmcnt(8)
	s_barrier
	s_waitcnt lgkmcnt(0)
	s_setprio 1
	s_setprio 0
	s_barrier
	s_and_b64 s[30:31], s[26:27], s[34:35]
	s_andn2_b64 vcc, exec, s[30:31]
	s_cbranch_vccnz .LBB0_1553
	ds_read2st64_b32 v[190:191], v179 offset1:2
	ds_read2st64_b32 v[192:193], v180 offset1:2
	s_waitcnt lgkmcnt(0)
	v_add_u32_e32 v184, v190, v1
	v_add_u32_e32 v190, v192, v181
	v_add_u32_e32 v192, v191, v1
	v_add_u32_e32 v194, v193, v181
.LBB0_1553:
	s_add_i32 s71, s71, 2
	s_add_u32 s30, s28, 0x100
	s_addc_u32 s31, s29, 0
	s_and_b64 s[36:37], s[34:35], exec
	s_cselect_b32 s36, 0, s30
	s_cselect_b32 s37, 0, s31
	s_add_u32 s36, s22, s36
	s_addc_u32 s37, s23, s37
	s_add_u32 s72, s69, s28
	s_addc_u32 s73, s70, s29
	s_and_b64 s[28:29], s[34:35], exec
	s_cselect_b32 s29, s67, s73
	s_cselect_b32 s28, s68, s72
	s_mov_b32 m0, s42
	v_add_u32_e32 v191, s57, v204
	v_lshl_add_u64 v[230:231], s[28:29], 0, v[188:189]
	v_add_u32_e32 v197, s57, v205
	ds_read_b128 v[214:217], v191
	ds_read_b128 v[222:225], v191 offset:2048
	ds_read_b128 v[218:221], v197
	ds_read_b128 v[226:229], v197 offset:2048
	global_load_lds_dwordx4 v[230:231], off
	v_lshl_add_u64 v[232:233], s[28:29], 0, v[186:187]
	s_mov_b32 m0, s43
	v_mfma_scale_f32_16x16x128_f8f6f4 v[174:177], v[2:9], v[26:33], v[174:177], v211, v210 op_sel_hi:[0,0,0]
	global_load_lds_dwordx4 v[232:233], off
	s_barrier
	v_mov_b32_e32 v193, v185
	v_mov_b32_e32 v195, v185
	v_mfma_scale_f32_16x16x128_f8f6f4 v[170:173], v[10:17], v[26:33], v[170:173], v211, v210 op_sel_hi:[0,0,0]
	v_mfma_scale_f32_16x16x128_f8f6f4 v[166:169], v[2:9], v[18:25], v[166:169], v211, v210 op_sel_hi:[0,0,0]
	v_mfma_scale_f32_16x16x128_f8f6f4 v[162:165], v[10:17], v[18:25], v[162:165], v211, v210 op_sel_hi:[0,0,0]
	v_mfma_scale_f32_16x16x128_f8f6f4 v[142:145], v[2:9], v[42:49], v[142:145], v211, v210 op_sel_hi:[0,0,0]
	v_mfma_scale_f32_16x16x128_f8f6f4 v[130:133], v[10:17], v[42:49], v[130:133], v211, v210 op_sel_hi:[0,0,0]
	v_mfma_scale_f32_16x16x128_f8f6f4 v[118:121], v[2:9], v[34:41], v[118:121], v211, v210 op_sel_hi:[0,0,0]
	v_mfma_scale_f32_16x16x128_f8f6f4 v[114:117], v[10:17], v[34:41], v[114:117], v211, v210 op_sel_hi:[0,0,0]
	s_setprio 1
	s_waitcnt lgkmcnt(0)
	v_mfma_scale_f32_16x16x128_f8f6f4 v[158:161], v[214:221], v[26:33], v[158:161], v211, v210 op_sel_hi:[0,0,0]
	v_mfma_scale_f32_16x16x128_f8f6f4 v[154:157], v[222:229], v[26:33], v[154:157], v211, v210 op_sel_hi:[0,0,0]
	ds_read_b128 v[26:29], v208 offset:18432
	ds_read_b128 v[30:33], v209 offset:18432
	v_mfma_scale_f32_16x16x128_f8f6f4 v[150:153], v[214:221], v[18:25], v[150:153], v211, v210 op_sel_hi:[0,0,0]
	v_mfma_scale_f32_16x16x128_f8f6f4 v[146:149], v[222:229], v[18:25], v[146:149], v211, v210 op_sel_hi:[0,0,0]
	ds_read_b128 v[18:21], v208 offset:16384
	ds_read_b128 v[22:25], v209 offset:16384
	v_mfma_scale_f32_16x16x128_f8f6f4 v[138:141], v[214:221], v[42:49], v[138:141], v211, v210 op_sel_hi:[0,0,0]
	v_mfma_scale_f32_16x16x128_f8f6f4 v[134:137], v[222:229], v[42:49], v[134:137], v211, v210 op_sel_hi:[0,0,0]
	ds_read_b128 v[42:45], v208 offset:22528
	ds_read_b128 v[46:49], v209 offset:22528
	v_mfma_scale_f32_16x16x128_f8f6f4 v[126:129], v[214:221], v[34:41], v[126:129], v211, v210 op_sel_hi:[0,0,0]
	v_mfma_scale_f32_16x16x128_f8f6f4 v[122:125], v[222:229], v[34:41], v[122:125], v211, v210 op_sel_hi:[0,0,0]
	ds_read_b128 v[34:37], v208 offset:20480
	ds_read_b128 v[38:41], v209 offset:20480
	s_setprio 0
	s_mov_b32 m0, s41
	s_barrier
	global_load_lds_dwordx4 v184, s[36:37]
	s_mov_b32 m0, s44
	v_mov_b32_e32 v191, v185
	global_load_lds_dwordx4 v190, s[36:37]
	s_barrier
	v_lshl_add_u64 v[234:235], s[36:37], 0, v[184:185]
	v_lshl_add_u64 v[236:237], s[36:37], 0, v[190:191]
	s_setprio 1
	s_waitcnt lgkmcnt(0)
	v_mfma_scale_f32_16x16x128_f8f6f4 v[110:113], v[2:9], v[18:25], v[110:113], v211, v210 op_sel_hi:[0,0,0]
	v_mfma_scale_f32_16x16x128_f8f6f4 v[102:105], v[10:17], v[18:25], v[102:105], v211, v210 op_sel_hi:[0,0,0]
	v_mfma_scale_f32_16x16x128_f8f6f4 v[94:97], v[2:9], v[26:33], v[94:97], v211, v210 op_sel_hi:[0,0,0]
	v_mfma_scale_f32_16x16x128_f8f6f4 v[86:89], v[10:17], v[26:33], v[86:89], v211, v210 op_sel_hi:[0,0,0]
	v_mfma_scale_f32_16x16x128_f8f6f4 v[78:81], v[2:9], v[34:41], v[78:81], v211, v210 op_sel_hi:[0,0,0]
	v_mfma_scale_f32_16x16x128_f8f6f4 v[70:73], v[10:17], v[34:41], v[70:73], v211, v210 op_sel_hi:[0,0,0]
	v_mfma_scale_f32_16x16x128_f8f6f4 v[62:65], v[2:9], v[42:49], v[62:65], v211, v210 op_sel_hi:[0,0,0]
	v_mfma_scale_f32_16x16x128_f8f6f4 v[54:57], v[10:17], v[42:49], v[54:57], v211, v210 op_sel_hi:[0,0,0]
	s_setprio 0
	s_barrier
	s_add_u32 s34, s28, 0x40000
	s_addc_u32 s35, s29, 0
	s_mov_b32 m0, s59
	v_lshl_add_u64 v[2:3], s[34:35], 0, v[188:189]
	global_load_lds_dwordx4 v[2:3], off
	v_lshl_add_u64 v[2:3], s[34:35], 0, v[186:187]
	s_mov_b32 m0, s60
	s_nop 0
	global_load_lds_dwordx4 v[2:3], off
	s_waitcnt vmcnt(6)
	s_barrier
	s_setprio 1
	v_mfma_scale_f32_16x16x128_f8f6f4 v[106:109], v[214:221], v[18:25], v[106:109], v211, v210 op_sel_hi:[0,0,0]
	v_mfma_scale_f32_16x16x128_f8f6f4 v[98:101], v[222:229], v[18:25], v[98:101], v211, v210 op_sel_hi:[0,0,0]
	ds_read_b128 v[18:21], v208 offset:32768
	ds_read_b128 v[22:25], v209 offset:32768
	v_mfma_scale_f32_16x16x128_f8f6f4 v[90:93], v[214:221], v[26:33], v[90:93], v211, v210 op_sel_hi:[0,0,0]
	v_mfma_scale_f32_16x16x128_f8f6f4 v[82:85], v[222:229], v[26:33], v[82:85], v211, v210 op_sel_hi:[0,0,0]
	ds_read_b128 v[26:29], v208 offset:34816
	ds_read_b128 v[30:33], v209 offset:34816
	v_mfma_scale_f32_16x16x128_f8f6f4 v[74:77], v[214:221], v[34:41], v[74:77], v211, v210 op_sel_hi:[0,0,0]
	v_mfma_scale_f32_16x16x128_f8f6f4 v[66:69], v[222:229], v[34:41], v[66:69], v211, v210 op_sel_hi:[0,0,0]
	ds_read_b128 v[34:37], v208 offset:36864
	ds_read_b128 v[38:41], v209 offset:36864
	v_mfma_scale_f32_16x16x128_f8f6f4 v[58:61], v[214:221], v[42:49], v[58:61], v211, v210 op_sel_hi:[0,0,0]
	v_mfma_scale_f32_16x16x128_f8f6f4 v[50:53], v[222:229], v[42:49], v[50:53], v211, v210 op_sel_hi:[0,0,0]
	ds_read_b128 v[42:45], v208 offset:38912
	ds_read_b128 v[46:49], v209 offset:38912
	s_setprio 0
	v_add_u32_e32 v6, s61, v204
	v_add_u32_e32 v14, s61, v205
	s_barrier
	ds_read_b128 v[2:5], v6
	ds_read_b128 v[10:13], v6 offset:2048
	ds_read_b128 v[6:9], v14
	ds_read_b128 v[14:17], v14 offset:2048
	s_mov_b32 m0, s45
	v_lshl_add_u64 v[214:215], s[36:37], 0, v[192:193]
	global_load_lds_dwordx4 v[214:215], off
	v_lshl_add_u64 v[214:215], s[36:37], 0, v[194:195]
	s_mov_b32 m0, s46
	s_nop 0
	global_load_lds_dwordx4 v[214:215], off
	s_waitcnt lgkmcnt(8)
	s_barrier
	s_setprio 1
	s_waitcnt lgkmcnt(0)
	v_mfma_scale_f32_16x16x128_f8f6f4 v[174:177], v[2:9], v[18:25], v[174:177], v211, v210 op_sel_hi:[0,0,0]
	v_mfma_scale_f32_16x16x128_f8f6f4 v[170:173], v[10:17], v[18:25], v[170:173], v211, v210 op_sel_hi:[0,0,0]
	v_mfma_scale_f32_16x16x128_f8f6f4 v[166:169], v[2:9], v[26:33], v[166:169], v211, v210 op_sel_hi:[0,0,0]
	v_mfma_scale_f32_16x16x128_f8f6f4 v[162:165], v[10:17], v[26:33], v[162:165], v211, v210 op_sel_hi:[0,0,0]
	v_mfma_scale_f32_16x16x128_f8f6f4 v[142:145], v[2:9], v[34:41], v[142:145], v211, v210 op_sel_hi:[0,0,0]
	v_mfma_scale_f32_16x16x128_f8f6f4 v[130:133], v[10:17], v[34:41], v[130:133], v211, v210 op_sel_hi:[0,0,0]
	v_mfma_scale_f32_16x16x128_f8f6f4 v[118:121], v[2:9], v[42:49], v[118:121], v211, v210 op_sel_hi:[0,0,0]
	v_mfma_scale_f32_16x16x128_f8f6f4 v[114:117], v[10:17], v[42:49], v[114:117], v211, v210 op_sel_hi:[0,0,0]
	s_setprio 0
	s_barrier
	s_mov_b32 m0, s63
	v_add_u32_e32 v191, s62, v204
	v_lshl_add_u64 v[230:231], v[230:231], 0, s[12:13]
	v_add_u32_e32 v193, s62, v205
	ds_read_b128 v[214:217], v191
	ds_read_b128 v[222:225], v191 offset:2048
	ds_read_b128 v[218:221], v193
	ds_read_b128 v[226:229], v193 offset:2048
	global_load_lds_dwordx4 v[230:231], off
	v_lshl_add_u64 v[230:231], v[232:233], 0, s[12:13]
	s_add_i32 m0, s63, 0x2000
	s_nop 0
	global_load_lds_dwordx4 v[230:231], off
	s_barrier
	s_setprio 1
	s_waitcnt lgkmcnt(0)
	v_mfma_scale_f32_16x16x128_f8f6f4 v[158:161], v[214:221], v[18:25], v[158:161], v211, v210 op_sel_hi:[0,0,0]
	v_mfma_scale_f32_16x16x128_f8f6f4 v[154:157], v[222:229], v[18:25], v[154:157], v211, v210 op_sel_hi:[0,0,0]
	ds_read_b128 v[18:21], v208 offset:49152
	ds_read_b128 v[22:25], v209 offset:49152
	v_mfma_scale_f32_16x16x128_f8f6f4 v[150:153], v[214:221], v[26:33], v[150:153], v211, v210 op_sel_hi:[0,0,0]
	v_mfma_scale_f32_16x16x128_f8f6f4 v[146:149], v[222:229], v[26:33], v[146:149], v211, v210 op_sel_hi:[0,0,0]
	ds_read_b128 v[26:29], v208 offset:51200
	ds_read_b128 v[30:33], v209 offset:51200
	v_mfma_scale_f32_16x16x128_f8f6f4 v[138:141], v[214:221], v[34:41], v[138:141], v211, v210 op_sel_hi:[0,0,0]
	v_mfma_scale_f32_16x16x128_f8f6f4 v[134:137], v[222:229], v[34:41], v[134:137], v211, v210 op_sel_hi:[0,0,0]
	ds_read_b128 v[34:37], v208 offset:53248
	ds_read_b128 v[38:41], v209 offset:53248
	v_mfma_scale_f32_16x16x128_f8f6f4 v[126:129], v[214:221], v[42:49], v[126:129], v211, v210 op_sel_hi:[0,0,0]
	v_mfma_scale_f32_16x16x128_f8f6f4 v[122:125], v[222:229], v[42:49], v[122:125], v211, v210 op_sel_hi:[0,0,0]
	ds_read_b128 v[42:45], v208 offset:55296
	ds_read_b128 v[46:49], v209 offset:55296
	s_setprio 0
	s_mov_b32 m0, s49
	v_lshl_add_u64 v[230:231], v[234:235], 0, s[12:13]
	s_barrier
	global_load_lds_dwordx4 v[230:231], off
	v_lshl_add_u64 v[230:231], v[236:237], 0, s[12:13]
	s_mov_b32 m0, s50
	s_nop 0
	global_load_lds_dwordx4 v[230:231], off
	s_barrier
	s_setprio 1
	s_waitcnt lgkmcnt(0)
	v_mfma_scale_f32_16x16x128_f8f6f4 v[110:113], v[2:9], v[18:25], v[110:113], v211, v210 op_sel_hi:[0,0,0]
	v_mfma_scale_f32_16x16x128_f8f6f4 v[102:105], v[10:17], v[18:25], v[102:105], v211, v210 op_sel_hi:[0,0,0]
	v_mfma_scale_f32_16x16x128_f8f6f4 v[94:97], v[2:9], v[26:33], v[94:97], v211, v210 op_sel_hi:[0,0,0]
	v_mfma_scale_f32_16x16x128_f8f6f4 v[86:89], v[10:17], v[26:33], v[86:89], v211, v210 op_sel_hi:[0,0,0]
	v_mfma_scale_f32_16x16x128_f8f6f4 v[78:81], v[2:9], v[34:41], v[78:81], v211, v210 op_sel_hi:[0,0,0]
	v_mfma_scale_f32_16x16x128_f8f6f4 v[70:73], v[10:17], v[34:41], v[70:73], v211, v210 op_sel_hi:[0,0,0]
	v_mfma_scale_f32_16x16x128_f8f6f4 v[62:65], v[2:9], v[42:49], v[62:65], v211, v210 op_sel_hi:[0,0,0]
	v_mfma_scale_f32_16x16x128_f8f6f4 v[54:57], v[10:17], v[42:49], v[54:57], v211, v210 op_sel_hi:[0,0,0]
	s_setprio 0
	s_barrier
	s_add_u32 s28, s28, 0x40080
	s_addc_u32 s29, s29, 0
	s_add_i32 s34, s62, s40
	v_lshl_add_u64 v[2:3], s[28:29], 0, v[188:189]
	s_mov_b32 m0, s34
	s_nop 0
	global_load_lds_dwordx4 v[2:3], off
	v_lshl_add_u64 v[2:3], s[28:29], 0, v[186:187]
	s_add_i32 m0, s34, 0x2000
	s_nop 0
	global_load_lds_dwordx4 v[2:3], off
	s_waitcnt vmcnt(6)
	s_barrier
	s_setprio 1
	v_mfma_scale_f32_16x16x128_f8f6f4 v[106:109], v[214:221], v[18:25], v[106:109], v211, v210 op_sel_hi:[0,0,0]
	ds_read_b128 v[2:5], v206
	ds_read_b128 v[10:13], v206 offset:2048
	ds_read_b128 v[6:9], v207
	ds_read_b128 v[14:17], v207 offset:2048
	v_mfma_scale_f32_16x16x128_f8f6f4 v[98:101], v[222:229], v[18:25], v[98:101], v211, v210 op_sel_hi:[0,0,0]
	ds_read_b128 v[18:21], v208 offset:2048
	ds_read_b128 v[22:25], v209 offset:2048
	v_mfma_scale_f32_16x16x128_f8f6f4 v[90:93], v[214:221], v[26:33], v[90:93], v211, v210 op_sel_hi:[0,0,0]
	v_mfma_scale_f32_16x16x128_f8f6f4 v[82:85], v[222:229], v[26:33], v[82:85], v211, v210 op_sel_hi:[0,0,0]
	ds_read_b128 v[26:29], v208
	ds_read_b128 v[30:33], v209
	v_mfma_scale_f32_16x16x128_f8f6f4 v[74:77], v[214:221], v[34:41], v[74:77], v211, v210 op_sel_hi:[0,0,0]
	v_mfma_scale_f32_16x16x128_f8f6f4 v[66:69], v[222:229], v[34:41], v[66:69], v211, v210 op_sel_hi:[0,0,0]
	ds_read_b128 v[34:37], v208 offset:6144
	ds_read_b128 v[38:41], v209 offset:6144
	v_mfma_scale_f32_16x16x128_f8f6f4 v[58:61], v[214:221], v[42:49], v[58:61], v211, v210 op_sel_hi:[0,0,0]
	v_mfma_scale_f32_16x16x128_f8f6f4 v[50:53], v[222:229], v[42:49], v[50:53], v211, v210 op_sel_hi:[0,0,0]
	ds_read_b128 v[42:45], v208 offset:4096
	ds_read_b128 v[46:49], v209 offset:4096
	s_setprio 0
	s_cmp_ge_i32 s71, s39
	s_barrier
	s_cbranch_scc1 .LBB0_1546
	s_mov_b64 s[28:29], s[30:31]
	s_branch .LBB0_1551

.LBB0_1668:
	s_waitcnt lgkmcnt(0)
	v_mov_b32_e32 v3, v200
	v_mov_b32_e32 v4, v201
	v_lshlrev_b32_e32 v2, 8, v183
	v_lshlrev_b32_e32 v5, 3, v4
	v_or_b32_e32 v2, s37, v2
	v_and_b32_e32 v5, -16, v5
	v_add_u32_e32 v2, v2, v5
	v_lshlrev_b32_e32 v5, 8, v182
	v_add_u32_e32 v5, s36, v5
	v_lshlrev_b32_e32 v4, 4, v4
	v_add_u32_e32 v10, v5, v3
	v_and_b32_e32 v11, 16, v4
	v_add_u32_e32 v4, v11, v10
	v_ashrrev_i32_e32 v5, 31, v4
	v_lshlrev_b64 v[4:5], 11, v[4:5]
	v_ashrrev_i32_e32 v3, 31, v2
	v_lshl_add_u64 v[4:5], s[14:15], 0, v[4:5]
	v_lshl_add_u64 v[8:9], v[4:5], 0, v[2:3]
	v_med3_f32 v4, v174, s47, v210
	v_med3_f32 v6, v175, s47, v210
	v_med3_f32 v5, v170, s47, v210
	v_med3_f32 v13, v171, s47, v210
	v_cvt_pk_fp8_f32 v4, v4, v6
	v_cvt_pk_fp8_f32 v5, v5, v13
	v_med3_f32 v7, v176, s47, v210
	v_med3_f32 v12, v177, s47, v210
	v_med3_f32 v6, v172, s47, v210
	v_med3_f32 v13, v173, s47, v210
	v_cvt_pk_fp8_f32 v4, v7, v12 op_sel:[0,0,1]
	v_cvt_pk_fp8_f32 v5, v6, v13 op_sel:[0,0,1]
	v_med3_f32 v6, v166, s47, v210
	v_med3_f32 v12, v167, s47, v210
	v_med3_f32 v7, v162, s47, v210
	v_cvt_pk_fp8_f32 v6, v6, v12
	v_med3_f32 v12, v163, s47, v210
	v_cvt_pk_fp8_f32 v7, v7, v12
	v_med3_f32 v13, v168, s47, v210
	v_med3_f32 v14, v169, s47, v210
	v_med3_f32 v12, v164, s47, v210
	v_cvt_pk_fp8_f32 v6, v13, v14 op_sel:[0,0,1]
	v_med3_f32 v13, v165, s47, v210
	v_cvt_pk_fp8_f32 v7, v12, v13 op_sel:[0,0,1]
	v_med3_f32 v13, v155, s47, v210
	v_permlane16_swap_b32_e32 v4, v6
	v_permlane16_swap_b32_e32 v5, v7
	global_store_dwordx4 v[8:9], v[4:7], off
	v_med3_f32 v12, v161, s47, v210
	v_med3_f32 v14, v153, s47, v210
	v_med3_f32 v4, v158, s47, v210
	v_med3_f32 v6, v159, s47, v210
	v_med3_f32 v5, v154, s47, v210
	v_cvt_pk_fp8_f32 v4, v4, v6
	v_cvt_pk_fp8_f32 v5, v5, v13
	v_med3_f32 v7, v160, s47, v210
	v_med3_f32 v6, v156, s47, v210
	v_med3_f32 v13, v157, s47, v210
	v_cvt_pk_fp8_f32 v4, v7, v12 op_sel:[0,0,1]
	v_cvt_pk_fp8_f32 v5, v6, v13 op_sel:[0,0,1]
	v_med3_f32 v6, v150, s47, v210
	v_med3_f32 v12, v151, s47, v210
	v_med3_f32 v7, v146, s47, v210
	v_cvt_pk_fp8_f32 v6, v6, v12
	v_med3_f32 v12, v147, s47, v210
	v_cvt_pk_fp8_f32 v7, v7, v12
	v_med3_f32 v13, v152, s47, v210
	v_med3_f32 v12, v148, s47, v210
	v_cvt_pk_fp8_f32 v6, v13, v14 op_sel:[0,0,1]
	v_med3_f32 v13, v149, s47, v210
	v_cvt_pk_fp8_f32 v7, v12, v13 op_sel:[0,0,1]
	v_or_b32_e32 v12, 32, v11
	v_permlane16_swap_b32_e32 v4, v6
	v_permlane16_swap_b32_e32 v5, v7
	global_store_dwordx4 v[8:9], v[4:7], off offset:128
	v_med3_f32 v14, v139, s47, v210
	v_med3_f32 v13, v145, s47, v210
	v_add_u32_e32 v4, v12, v10
	v_ashrrev_i32_e32 v5, 31, v4
	v_lshlrev_b64 v[4:5], 11, v[4:5]
	v_lshl_add_u64 v[4:5], s[14:15], 0, v[4:5]
	v_lshl_add_u64 v[8:9], v[4:5], 0, v[2:3]
	v_med3_f32 v4, v142, s47, v210
	v_med3_f32 v6, v143, s47, v210
	v_med3_f32 v5, v138, s47, v210
	v_cvt_pk_fp8_f32 v4, v4, v6
	v_cvt_pk_fp8_f32 v5, v5, v14
	v_med3_f32 v7, v144, s47, v210
	v_med3_f32 v6, v140, s47, v210
	v_med3_f32 v14, v141, s47, v210
	v_cvt_pk_fp8_f32 v4, v7, v13 op_sel:[0,0,1]
	v_cvt_pk_fp8_f32 v5, v6, v14 op_sel:[0,0,1]
	v_med3_f32 v6, v134, s47, v210
	v_med3_f32 v13, v135, s47, v210
	v_med3_f32 v7, v122, s47, v210
	v_cvt_pk_fp8_f32 v6, v6, v13
	v_med3_f32 v13, v123, s47, v210
	v_cvt_pk_fp8_f32 v7, v7, v13
	v_med3_f32 v14, v136, s47, v210
	v_med3_f32 v15, v137, s47, v210
	v_med3_f32 v13, v124, s47, v210
	v_cvt_pk_fp8_f32 v6, v14, v15 op_sel:[0,0,1]
	v_med3_f32 v14, v125, s47, v210
	v_cvt_pk_fp8_f32 v7, v13, v14 op_sel:[0,0,1]
	v_med3_f32 v14, v127, s47, v210
	v_permlane16_swap_b32_e32 v4, v6
	v_permlane16_swap_b32_e32 v5, v7
	global_store_dwordx4 v[8:9], v[4:7], off
	v_med3_f32 v13, v133, s47, v210
	v_med3_f32 v15, v121, s47, v210
	v_med3_f32 v4, v130, s47, v210
	v_med3_f32 v6, v131, s47, v210
	v_med3_f32 v5, v126, s47, v210
	v_cvt_pk_fp8_f32 v4, v4, v6
	v_cvt_pk_fp8_f32 v5, v5, v14
	v_med3_f32 v7, v132, s47, v210
	v_med3_f32 v6, v128, s47, v210
	v_med3_f32 v14, v129, s47, v210
	v_cvt_pk_fp8_f32 v4, v7, v13 op_sel:[0,0,1]
	v_cvt_pk_fp8_f32 v5, v6, v14 op_sel:[0,0,1]
	v_med3_f32 v6, v118, s47, v210
	v_med3_f32 v13, v119, s47, v210
	v_med3_f32 v7, v114, s47, v210
	v_cvt_pk_fp8_f32 v6, v6, v13
	v_med3_f32 v13, v115, s47, v210
	v_cvt_pk_fp8_f32 v7, v7, v13
	v_med3_f32 v14, v120, s47, v210
	v_med3_f32 v13, v116, s47, v210
	v_cvt_pk_fp8_f32 v6, v14, v15 op_sel:[0,0,1]
	v_med3_f32 v14, v117, s47, v210
	v_cvt_pk_fp8_f32 v7, v13, v14 op_sel:[0,0,1]
	v_add_u32_e32 v10, 0x80, v10
	v_permlane16_swap_b32_e32 v4, v6
	v_permlane16_swap_b32_e32 v5, v7
	global_store_dwordx4 v[8:9], v[4:7], off offset:128
	v_med3_f32 v13, v107, s47, v210
	v_med3_f32 v14, v105, s47, v210
	v_add_u32_e32 v4, v10, v11
	v_ashrrev_i32_e32 v5, 31, v4
	v_lshlrev_b64 v[4:5], 11, v[4:5]
	v_lshl_add_u64 v[4:5], s[14:15], 0, v[4:5]
	v_lshl_add_u64 v[8:9], v[4:5], 0, v[2:3]
	v_med3_f32 v4, v110, s47, v210
	v_med3_f32 v6, v111, s47, v210
	v_med3_f32 v5, v106, s47, v210
	v_cvt_pk_fp8_f32 v4, v4, v6
	v_cvt_pk_fp8_f32 v5, v5, v13
	v_med3_f32 v7, v112, s47, v210
	v_med3_f32 v11, v113, s47, v210
	v_med3_f32 v6, v108, s47, v210
	v_med3_f32 v13, v109, s47, v210
	v_cvt_pk_fp8_f32 v4, v7, v11 op_sel:[0,0,1]
	v_cvt_pk_fp8_f32 v5, v6, v13 op_sel:[0,0,1]
	v_med3_f32 v6, v102, s47, v210
	v_med3_f32 v11, v103, s47, v210
	v_med3_f32 v7, v98, s47, v210
	v_cvt_pk_fp8_f32 v6, v6, v11
	v_med3_f32 v11, v99, s47, v210
	v_cvt_pk_fp8_f32 v7, v7, v11
	v_med3_f32 v13, v104, s47, v210
	v_med3_f32 v11, v100, s47, v210
	v_cvt_pk_fp8_f32 v6, v13, v14 op_sel:[0,0,1]
	v_med3_f32 v13, v101, s47, v210
	v_cvt_pk_fp8_f32 v7, v11, v13 op_sel:[0,0,1]
	v_med3_f32 v13, v91, s47, v210
	v_permlane16_swap_b32_e32 v4, v6
	v_permlane16_swap_b32_e32 v5, v7
	global_store_dwordx4 v[8:9], v[4:7], off
	v_med3_f32 v11, v97, s47, v210
	v_med3_f32 v14, v89, s47, v210
	v_med3_f32 v4, v94, s47, v210
	v_med3_f32 v6, v95, s47, v210
	v_med3_f32 v5, v90, s47, v210
	v_cvt_pk_fp8_f32 v4, v4, v6
	v_cvt_pk_fp8_f32 v5, v5, v13
	v_med3_f32 v7, v96, s47, v210
	v_med3_f32 v6, v92, s47, v210
	v_med3_f32 v13, v93, s47, v210
	v_cvt_pk_fp8_f32 v4, v7, v11 op_sel:[0,0,1]
	v_cvt_pk_fp8_f32 v5, v6, v13 op_sel:[0,0,1]
	v_med3_f32 v6, v86, s47, v210
	v_med3_f32 v11, v87, s47, v210
	v_med3_f32 v7, v82, s47, v210
	v_cvt_pk_fp8_f32 v6, v6, v11
	v_med3_f32 v11, v83, s47, v210
	v_cvt_pk_fp8_f32 v7, v7, v11
	v_med3_f32 v13, v88, s47, v210
	v_med3_f32 v11, v84, s47, v210
	v_cvt_pk_fp8_f32 v6, v13, v14 op_sel:[0,0,1]
	v_med3_f32 v13, v85, s47, v210
	v_cvt_pk_fp8_f32 v7, v11, v13 op_sel:[0,0,1]
	s_cmp_eq_u32 s40, s30
	v_permlane16_swap_b32_e32 v4, v6
	v_permlane16_swap_b32_e32 v5, v7
	global_store_dwordx4 v[8:9], v[4:7], off offset:128
	v_med3_f32 v9, v75, s47, v210
	v_med3_f32 v8, v81, s47, v210
	v_add_u32_e32 v4, v12, v10
	v_ashrrev_i32_e32 v5, 31, v4
	v_lshlrev_b64 v[4:5], 11, v[4:5]
	v_lshl_add_u64 v[4:5], s[14:15], 0, v[4:5]
	v_lshl_add_u64 v[6:7], v[4:5], 0, v[2:3]
	v_med3_f32 v2, v78, s47, v210
	v_med3_f32 v4, v79, s47, v210
	v_med3_f32 v3, v74, s47, v210
	v_cvt_pk_fp8_f32 v2, v2, v4
	v_cvt_pk_fp8_f32 v3, v3, v9
	v_med3_f32 v5, v80, s47, v210
	v_med3_f32 v4, v76, s47, v210
	v_med3_f32 v9, v77, s47, v210
	v_cvt_pk_fp8_f32 v2, v5, v8 op_sel:[0,0,1]
	v_cvt_pk_fp8_f32 v3, v4, v9 op_sel:[0,0,1]
	v_med3_f32 v4, v70, s47, v210
	v_med3_f32 v8, v71, s47, v210
	v_med3_f32 v5, v66, s47, v210
	v_cvt_pk_fp8_f32 v4, v4, v8
	v_med3_f32 v8, v67, s47, v210
	v_cvt_pk_fp8_f32 v5, v5, v8
	v_med3_f32 v9, v72, s47, v210
	v_med3_f32 v10, v73, s47, v210
	v_med3_f32 v8, v68, s47, v210
	v_cvt_pk_fp8_f32 v4, v9, v10 op_sel:[0,0,1]
	v_med3_f32 v9, v69, s47, v210
	v_cvt_pk_fp8_f32 v5, v8, v9 op_sel:[0,0,1]
	v_med3_f32 v9, v59, s47, v210
	v_permlane16_swap_b32_e32 v2, v4
	v_permlane16_swap_b32_e32 v3, v5
	global_store_dwordx4 v[6:7], v[2:5], off
	v_med3_f32 v8, v65, s47, v210
	v_med3_f32 v10, v57, s47, v210
	v_med3_f32 v2, v62, s47, v210
	v_med3_f32 v4, v63, s47, v210
	v_med3_f32 v3, v58, s47, v210
	v_cvt_pk_fp8_f32 v2, v2, v4
	v_cvt_pk_fp8_f32 v3, v3, v9
	v_med3_f32 v5, v64, s47, v210
	v_med3_f32 v4, v60, s47, v210
	v_med3_f32 v9, v61, s47, v210
	v_cvt_pk_fp8_f32 v2, v5, v8 op_sel:[0,0,1]
	v_cvt_pk_fp8_f32 v3, v4, v9 op_sel:[0,0,1]
	v_med3_f32 v4, v54, s47, v210
	v_med3_f32 v8, v55, s47, v210
	v_med3_f32 v5, v50, s47, v210
	v_cvt_pk_fp8_f32 v4, v4, v8
	v_med3_f32 v8, v51, s47, v210
	v_cvt_pk_fp8_f32 v5, v5, v8
	v_med3_f32 v9, v56, s47, v210
	v_med3_f32 v8, v52, s47, v210
	v_cvt_pk_fp8_f32 v4, v9, v10 op_sel:[0,0,1]
	v_med3_f32 v9, v53, s47, v210
	v_cvt_pk_fp8_f32 v5, v8, v9 op_sel:[0,0,1]
	v_mov_b32_e32 v183, s16
	v_permlane16_swap_b32_e32 v2, v4
	v_permlane16_swap_b32_e32 v3, v5
	v_mov_b32_e32 v182, v178
	s_mov_b64 s[22:23], s[18:19]
	global_store_dwordx4 v[6:7], v[2:5], off offset:128
	s_cbranch_scc1 .LBB0_1677

.Lmy_pl3_1675:
	s_add_i32 s59, s59, 2
	s_add_u32 s24, s22, 0x100
	s_addc_u32 s25, s23, 0
	s_and_b64 s[28:29], s[26:27], exec
	s_cselect_b32 s28, 0, s24
	s_cselect_b32 s29, 0, s25
	s_add_u32 s28, s12, s28
	s_addc_u32 s29, s13, s29
	s_add_u32 s60, s57, s22
	s_addc_u32 s61, s58, s23
	s_and_b64 s[22:23], s[26:27], exec
	s_cselect_b32 s23, s55, s61
	s_cselect_b32 s22, s56, s60
	s_mov_b32 m0, s5
	s_waitcnt lgkmcnt(0)
	v_mfma_scale_f32_16x16x128_f8f6f4 v[222:225], v[2:9], v[42:49], 0, v209, v208 op_sel_hi:[0,0,0]
	v_lshl_add_u64 v[238:239], s[22:23], 0, v[188:189]
	v_add_u32_e32 v191, s46, v203
	v_lshl_add_u64 v[240:241], s[22:23], 0, v[186:187]
	v_mov_b32_e32 v193, v185
	v_mov_b32_e32 v195, v185
	s_nop 1
	v_add_u32_e32 v142, s46, v202
	v_mfma_scale_f32_16x16x128_f8f6f4 v[226:229], v[10:17], v[42:49], 0, v209, v208 op_sel_hi:[0,0,0]
	s_nop 6
	ds_read_b128 v[138:141], v142
	ds_read_b128 v[214:217], v142 offset:2048
	ds_read_b128 v[142:145], v191
	ds_read_b128 v[218:221], v191 offset:2048
	global_load_lds_dwordx4 v[238:239], off
	s_mov_b32 m0, s31
	s_nop 0
	global_load_lds_dwordx4 v[240:241], off
	v_mfma_scale_f32_16x16x128_f8f6f4 v[174:177], v[2:9], v[26:33], 0, v209, v208 op_sel_hi:[0,0,0]
	s_barrier
	v_mfma_scale_f32_16x16x128_f8f6f4 v[170:173], v[10:17], v[26:33], 0, v209, v208 op_sel_hi:[0,0,0]
	v_mfma_scale_f32_16x16x128_f8f6f4 v[166:169], v[2:9], v[18:25], 0, v209, v208 op_sel_hi:[0,0,0]
	v_mfma_scale_f32_16x16x128_f8f6f4 v[162:165], v[10:17], v[18:25], 0, v209, v208 op_sel_hi:[0,0,0]
	v_mfma_scale_f32_16x16x128_f8f6f4 v[134:137], v[2:9], v[34:41], 0, v209, v208 op_sel_hi:[0,0,0]
	v_mfma_scale_f32_16x16x128_f8f6f4 v[122:125], v[10:17], v[34:41], 0, v209, v208 op_sel_hi:[0,0,0]
	s_setprio 1
	s_waitcnt lgkmcnt(0)
	v_mfma_scale_f32_16x16x128_f8f6f4 v[158:161], v[138:145], v[26:33], 0, v209, v208 op_sel_hi:[0,0,0]
	v_mfma_scale_f32_16x16x128_f8f6f4 v[154:157], v[214:221], v[26:33], 0, v209, v208 op_sel_hi:[0,0,0]
	ds_read_b128 v[26:29], v206 offset:18432
	ds_read_b128 v[30:33], v207 offset:18432
	v_mfma_scale_f32_16x16x128_f8f6f4 v[150:153], v[138:145], v[18:25], 0, v209, v208 op_sel_hi:[0,0,0]
	v_mfma_scale_f32_16x16x128_f8f6f4 v[146:149], v[214:221], v[18:25], 0, v209, v208 op_sel_hi:[0,0,0]
	ds_read_b128 v[18:21], v206 offset:16384
	ds_read_b128 v[22:25], v207 offset:16384
	v_mfma_scale_f32_16x16x128_f8f6f4 v[130:133], v[138:145], v[42:49], 0, v209, v208 op_sel_hi:[0,0,0]
	v_mfma_scale_f32_16x16x128_f8f6f4 v[126:129], v[214:221], v[42:49], 0, v209, v208 op_sel_hi:[0,0,0]
	ds_read_b128 v[42:45], v206 offset:22528
	ds_read_b128 v[46:49], v207 offset:22528
	v_mfma_scale_f32_16x16x128_f8f6f4 v[118:121], v[138:145], v[34:41], 0, v209, v208 op_sel_hi:[0,0,0]
	v_mfma_scale_f32_16x16x128_f8f6f4 v[114:117], v[214:221], v[34:41], 0, v209, v208 op_sel_hi:[0,0,0]
	ds_read_b128 v[34:37], v206 offset:20480
	ds_read_b128 v[38:41], v207 offset:20480
	s_setprio 0
	s_mov_b32 m0, s4
	s_barrier
	global_load_lds_dwordx4 v184, s[28:29]
	s_mov_b32 m0, s33
	v_mov_b32_e32 v191, v185
	global_load_lds_dwordx4 v190, s[28:29]
	s_barrier
	v_lshl_add_u64 v[242:243], s[28:29], 0, v[184:185]
	v_lshl_add_u64 v[244:245], s[28:29], 0, v[190:191]
	s_setprio 1
	s_waitcnt lgkmcnt(0)
	v_mfma_scale_f32_16x16x128_f8f6f4 v[110:113], v[2:9], v[18:25], 0, v209, v208 op_sel_hi:[0,0,0]
	v_mfma_scale_f32_16x16x128_f8f6f4 v[106:109], v[10:17], v[18:25], 0, v209, v208 op_sel_hi:[0,0,0]
	v_mfma_scale_f32_16x16x128_f8f6f4 v[102:105], v[2:9], v[26:33], 0, v209, v208 op_sel_hi:[0,0,0]
	v_mfma_scale_f32_16x16x128_f8f6f4 v[98:101], v[10:17], v[26:33], 0, v209, v208 op_sel_hi:[0,0,0]
	v_mfma_scale_f32_16x16x128_f8f6f4 v[78:81], v[2:9], v[34:41], 0, v209, v208 op_sel_hi:[0,0,0]
	v_mfma_scale_f32_16x16x128_f8f6f4 v[74:77], v[10:17], v[34:41], 0, v209, v208 op_sel_hi:[0,0,0]
	v_mfma_scale_f32_16x16x128_f8f6f4 v[70:73], v[2:9], v[42:49], 0, v209, v208 op_sel_hi:[0,0,0]
	v_mfma_scale_f32_16x16x128_f8f6f4 v[66:69], v[10:17], v[42:49], 0, v209, v208 op_sel_hi:[0,0,0]
	s_setprio 0
	s_barrier
	s_add_u32 s26, s22, 0x10000
	s_addc_u32 s27, s23, 0
	s_mov_b32 m0, s48
	v_lshl_add_u64 v[2:3], s[26:27], 0, v[188:189]
	global_load_lds_dwordx4 v[2:3], off
	v_lshl_add_u64 v[2:3], s[26:27], 0, v[186:187]
	s_mov_b32 m0, s49
	s_nop 0
	global_load_lds_dwordx4 v[2:3], off
	s_waitcnt vmcnt(6)
	s_barrier
	s_setprio 1
	v_mfma_scale_f32_16x16x128_f8f6f4 v[94:97], v[138:145], v[18:25], 0, v209, v208 op_sel_hi:[0,0,0]
	v_mfma_scale_f32_16x16x128_f8f6f4 v[90:93], v[214:221], v[18:25], 0, v209, v208 op_sel_hi:[0,0,0]
	ds_read_b128 v[18:21], v206 offset:32768
	ds_read_b128 v[22:25], v207 offset:32768
	v_mfma_scale_f32_16x16x128_f8f6f4 v[86:89], v[138:145], v[26:33], 0, v209, v208 op_sel_hi:[0,0,0]
	v_mfma_scale_f32_16x16x128_f8f6f4 v[82:85], v[214:221], v[26:33], 0, v209, v208 op_sel_hi:[0,0,0]
	ds_read_b128 v[26:29], v206 offset:34816
	ds_read_b128 v[30:33], v207 offset:34816
	v_mfma_scale_f32_16x16x128_f8f6f4 v[62:65], v[138:145], v[34:41], 0, v209, v208 op_sel_hi:[0,0,0]
	v_mfma_scale_f32_16x16x128_f8f6f4 v[58:61], v[214:221], v[34:41], 0, v209, v208 op_sel_hi:[0,0,0]
	ds_read_b128 v[34:37], v206 offset:36864
	ds_read_b128 v[38:41], v207 offset:36864
	v_mfma_scale_f32_16x16x128_f8f6f4 v[230:233], v[138:145], v[42:49], 0, v209, v208 op_sel_hi:[0,0,0]
	v_mfma_scale_f32_16x16x128_f8f6f4 v[234:237], v[214:221], v[42:49], 0, v209, v208 op_sel_hi:[0,0,0]
	ds_read_b128 v[42:45], v206 offset:38912
	ds_read_b128 v[46:49], v207 offset:38912
	s_setprio 0
	v_add_u32_e32 v6, s50, v202
	v_add_u32_e32 v14, s50, v203
	s_barrier
	ds_read_b128 v[2:5], v6
	ds_read_b128 v[10:13], v6 offset:2048
	ds_read_b128 v[6:9], v14
	ds_read_b128 v[14:17], v14 offset:2048
	s_mov_b32 m0, s34
	v_lshl_add_u64 v[50:51], s[28:29], 0, v[192:193]
	global_load_lds_dwordx4 v[50:51], off
	v_lshl_add_u64 v[50:51], s[28:29], 0, v[194:195]
	s_mov_b32 m0, s35
	s_nop 0
	global_load_lds_dwordx4 v[50:51], off
	s_waitcnt lgkmcnt(8)
	s_barrier
	s_setprio 1
	s_waitcnt lgkmcnt(0)
	v_mfma_scale_f32_16x16x128_f8f6f4 v[174:177], v[2:9], v[18:25], v[174:177], v209, v208 op_sel_hi:[0,0,0]
	v_mfma_scale_f32_16x16x128_f8f6f4 v[170:173], v[10:17], v[18:25], v[170:173], v209, v208 op_sel_hi:[0,0,0]
	v_mfma_scale_f32_16x16x128_f8f6f4 v[166:169], v[2:9], v[26:33], v[166:169], v209, v208 op_sel_hi:[0,0,0]
	v_mfma_scale_f32_16x16x128_f8f6f4 v[162:165], v[10:17], v[26:33], v[162:165], v209, v208 op_sel_hi:[0,0,0]
	v_mfma_scale_f32_16x16x128_f8f6f4 v[142:145], v[2:9], v[34:41], v[222:225], v209, v208 op_sel_hi:[0,0,0]
	v_mfma_scale_f32_16x16x128_f8f6f4 v[138:141], v[10:17], v[34:41], v[226:229], v209, v208 op_sel_hi:[0,0,0]
	v_mfma_scale_f32_16x16x128_f8f6f4 v[134:137], v[2:9], v[42:49], v[134:137], v209, v208 op_sel_hi:[0,0,0]
	v_mfma_scale_f32_16x16x128_f8f6f4 v[122:125], v[10:17], v[42:49], v[122:125], v209, v208 op_sel_hi:[0,0,0]
	s_setprio 0
	s_barrier
	s_mov_b32 m0, s52
	v_add_u32_e32 v54, s51, v202
	v_lshl_add_u64 v[222:223], v[238:239], 0, s[8:9]
	v_add_u32_e32 v191, s51, v203
	ds_read_b128 v[50:53], v54
	ds_read_b128 v[214:217], v54 offset:2048
	ds_read_b128 v[54:57], v191
	ds_read_b128 v[218:221], v191 offset:2048
	global_load_lds_dwordx4 v[222:223], off
	v_lshl_add_u64 v[222:223], v[240:241], 0, s[8:9]
	s_mov_b32 m0, s53
	s_nop 0
	global_load_lds_dwordx4 v[222:223], off
	s_barrier
	s_setprio 1
	s_waitcnt lgkmcnt(0)
	v_mfma_scale_f32_16x16x128_f8f6f4 v[158:161], v[50:57], v[18:25], v[158:161], v209, v208 op_sel_hi:[0,0,0]
	v_mfma_scale_f32_16x16x128_f8f6f4 v[154:157], v[214:221], v[18:25], v[154:157], v209, v208 op_sel_hi:[0,0,0]
	ds_read_b128 v[18:21], v206 offset:49152
	ds_read_b128 v[22:25], v207 offset:49152
	v_mfma_scale_f32_16x16x128_f8f6f4 v[150:153], v[50:57], v[26:33], v[150:153], v209, v208 op_sel_hi:[0,0,0]
	v_mfma_scale_f32_16x16x128_f8f6f4 v[146:149], v[214:221], v[26:33], v[146:149], v209, v208 op_sel_hi:[0,0,0]
	ds_read_b128 v[26:29], v206 offset:51200
	ds_read_b128 v[30:33], v207 offset:51200
	v_mfma_scale_f32_16x16x128_f8f6f4 v[130:133], v[50:57], v[34:41], v[130:133], v209, v208 op_sel_hi:[0,0,0]
	v_mfma_scale_f32_16x16x128_f8f6f4 v[126:129], v[214:221], v[34:41], v[126:129], v209, v208 op_sel_hi:[0,0,0]
	ds_read_b128 v[34:37], v206 offset:53248
	ds_read_b128 v[38:41], v207 offset:53248
	v_mfma_scale_f32_16x16x128_f8f6f4 v[118:121], v[50:57], v[42:49], v[118:121], v209, v208 op_sel_hi:[0,0,0]
	v_mfma_scale_f32_16x16x128_f8f6f4 v[114:117], v[214:221], v[42:49], v[114:117], v209, v208 op_sel_hi:[0,0,0]
	ds_read_b128 v[42:45], v206 offset:55296
	ds_read_b128 v[46:49], v207 offset:55296
	s_setprio 0
	s_mov_b32 m0, s38
	v_lshl_add_u64 v[222:223], v[242:243], 0, s[8:9]
	s_barrier
	global_load_lds_dwordx4 v[222:223], off
	v_lshl_add_u64 v[222:223], v[244:245], 0, s[8:9]
	s_mov_b32 m0, s39
	s_nop 0
	global_load_lds_dwordx4 v[222:223], off
	s_barrier
	s_setprio 1
	s_waitcnt lgkmcnt(0)
	v_mfma_scale_f32_16x16x128_f8f6f4 v[110:113], v[2:9], v[18:25], v[110:113], v209, v208 op_sel_hi:[0,0,0]
	v_mfma_scale_f32_16x16x128_f8f6f4 v[106:109], v[10:17], v[18:25], v[106:109], v209, v208 op_sel_hi:[0,0,0]
	v_mfma_scale_f32_16x16x128_f8f6f4 v[102:105], v[2:9], v[26:33], v[102:105], v209, v208 op_sel_hi:[0,0,0]
	v_mfma_scale_f32_16x16x128_f8f6f4 v[98:101], v[10:17], v[26:33], v[98:101], v209, v208 op_sel_hi:[0,0,0]
	v_mfma_scale_f32_16x16x128_f8f6f4 v[78:81], v[2:9], v[34:41], v[78:81], v209, v208 op_sel_hi:[0,0,0]
	v_mfma_scale_f32_16x16x128_f8f6f4 v[74:77], v[10:17], v[34:41], v[74:77], v209, v208 op_sel_hi:[0,0,0]
	v_mfma_scale_f32_16x16x128_f8f6f4 v[70:73], v[2:9], v[42:49], v[70:73], v209, v208 op_sel_hi:[0,0,0]
	v_mfma_scale_f32_16x16x128_f8f6f4 v[66:69], v[10:17], v[42:49], v[66:69], v209, v208 op_sel_hi:[0,0,0]
	s_setprio 0
	s_barrier
	s_add_u32 s22, s22, 0x10080
	s_addc_u32 s23, s23, 0
	s_mov_b32 m0, s54
	v_lshl_add_u64 v[2:3], s[22:23], 0, v[188:189]
	global_load_lds_dwordx4 v[2:3], off
	v_lshl_add_u64 v[2:3], s[22:23], 0, v[186:187]
	s_add_i32 m0, s54, 0x2000
	s_nop 0
	global_load_lds_dwordx4 v[2:3], off
	s_waitcnt vmcnt(6)
	s_barrier
	s_setprio 1
	v_mfma_scale_f32_16x16x128_f8f6f4 v[94:97], v[50:57], v[18:25], v[94:97], v209, v208 op_sel_hi:[0,0,0]
	ds_read_b128 v[2:5], v204
	ds_read_b128 v[10:13], v204 offset:2048
	ds_read_b128 v[6:9], v205
	ds_read_b128 v[14:17], v205 offset:2048
	v_mfma_scale_f32_16x16x128_f8f6f4 v[90:93], v[214:221], v[18:25], v[90:93], v209, v208 op_sel_hi:[0,0,0]
	ds_read_b128 v[18:21], v206 offset:2048
	ds_read_b128 v[22:25], v207 offset:2048
	v_mfma_scale_f32_16x16x128_f8f6f4 v[86:89], v[50:57], v[26:33], v[86:89], v209, v208 op_sel_hi:[0,0,0]
	v_mfma_scale_f32_16x16x128_f8f6f4 v[82:85], v[214:221], v[26:33], v[82:85], v209, v208 op_sel_hi:[0,0,0]
	ds_read_b128 v[26:29], v206
	ds_read_b128 v[30:33], v207
	v_mfma_scale_f32_16x16x128_f8f6f4 v[62:65], v[50:57], v[34:41], v[62:65], v209, v208 op_sel_hi:[0,0,0]
	v_mfma_scale_f32_16x16x128_f8f6f4 v[58:61], v[214:221], v[34:41], v[58:61], v209, v208 op_sel_hi:[0,0,0]
	ds_read_b128 v[34:37], v206 offset:6144
	ds_read_b128 v[38:41], v207 offset:6144
	v_mfma_scale_f32_16x16x128_f8f6f4 v[54:57], v[50:57], v[42:49], v[230:233], v209, v208 op_sel_hi:[0,0,0]
	v_mfma_scale_f32_16x16x128_f8f6f4 v[50:53], v[214:221], v[42:49], v[234:237], v209, v208 op_sel_hi:[0,0,0]
	ds_read_b128 v[42:45], v206 offset:4096
	ds_read_b128 v[46:49], v207 offset:4096
	s_setprio 0
	s_cmp_ge_i32 s59, s1
	s_barrier
	s_cbranch_scc1 .LBB0_1668
	s_mov_b64 s[22:23], s[24:25]
	s_branch .LBB0_1673
.LBB0_1673:
	s_cmp_eq_u32 s41, s59
	s_cselect_b64 s[26:27], -1, 0
	s_add_u32 s24, s42, s22
	s_addc_u32 s25, s43, s23
	s_mov_b32 m0, s44
	global_load_lds_dwordx4 v192, s[24:25]
	s_mov_b32 m0, s45
	s_nop 0
	global_load_lds_dwordx4 v194, s[24:25]
	s_waitcnt lgkmcnt(8)
	s_barrier
	s_waitcnt lgkmcnt(0)
	s_setprio 1
	s_setprio 0
	s_barrier
	s_and_b64 s[24:25], s[20:21], s[26:27]
	s_andn2_b64 vcc, exec, s[24:25]
	s_cbranch_vccnz .LBB0_1675
	ds_read2st64_b32 v[190:191], v179 offset1:2
	ds_read2st64_b32 v[192:193], v180 offset1:2
	s_waitcnt lgkmcnt(0)
	v_add_u32_e32 v184, v190, v1
	v_add_u32_e32 v190, v192, v181
	v_add_u32_e32 v192, v191, v1
	v_add_u32_e32 v194, v193, v181
